# cache-policy lever, part 6: nt hint on the once-read f32 weight loads of the set-up phase (adaLN weights and the small-weight conversion)
# baseline (speedup 1.0000x reference)
; __device__ __forceinline__ const float* IN(KArgs a, int i) { return (const float*)a->in[i]; }
; #define a launder(kargs)
; __device__ __forceinline__ void p0_phase(Frame& F, KArgs a) {
;     ...
;     for (int i = F.tid; i < 9 * 1024; i += 512) { const float v = (i < 8192) ? IN(a, I_C)[i] : IN(a, I_CCTX)[i - 8192]; sc[i] = v / (1.f + __expf(-v)); }
.LBB0_15:
	s_or_b64 exec, exec, s[18:19]
	global_load_dword v6, v[6:7], off nt
	v_add_u32_e32 v8, 0x200, v4
	v_cmp_lt_i32_e32 vcc, s21, v4
	s_or_b64 s[6:7], vcc, s[6:7]
	v_lshl_add_u64 v[2:3], v[2:3], 0, s[10:11]
	s_waitcnt vmcnt(0)
	v_mul_f32_e32 v7, 0xbfb8aa3b, v6
	v_exp_f32_e32 v7, v7
	s_nop 0
	v_add_f32_e32 v4, 1.0, v7
	v_div_scale_f32 v7, s[18:19], v4, v4, v6
	v_rcp_f32_e32 v9, v7
	v_div_scale_f32 v10, vcc, v6, v4, v6
	v_fma_f32 v11, -v7, v9, 1.0
	v_fmac_f32_e32 v9, v11, v9
	v_mul_f32_e32 v11, v10, v9
	v_fma_f32 v12, -v7, v11, v10
	v_fmac_f32_e32 v11, v12, v9
	v_fma_f32 v7, -v7, v11, v10
	v_div_fmas_f32 v7, v7, v9, v11
	v_div_fixup_f32 v4, v7, v4, v6
	ds_write_b32 v1, v4
	v_add_u32_e32 v1, 0x800, v1
	v_mov_b32_e32 v4, v8
	s_andn2_b64 exec, exec, s[6:7]
	s_cbranch_execz .LBB0_20

; #define LAS __attribute__((address_space(3)))
; __device__ __forceinline__ void p0_phase(Frame& F, KArgs a) {
;     ...
; #pragma unroll 1
;         for (int k0 = 0; k0 < 64; k0 += 32) {
;             float w[32];
; #pragma unroll
;             for (int j = 0; j < 32; ++j) w[j] = wp[(size_t)(kb + k0 + j) * 6144];
; #pragma unroll
;             for (int k = 0; k < 32; k += 4)
; #pragma unroll
;                 for (int s = 0; s < 9; ++s) { const f32x4 sv = *(const LAS f32x4*)(sc + s * 1024 + kb + k0 + k); acc[s] += sv[0] * w[k] + sv[1] * w[k + 1] + sv[2] * w[k + 2] + sv[3] * w[k + 3]; }
;         }
.LBB0_24:
	v_lshl_add_u32 v116, s19, 2, v112
	ds_read_b128 v[18:21], v116 offset:20480
	ds_read_b128 v[38:41], v116 offset:24576
	ds_read_b128 v[26:29], v116 offset:4096
	ds_read_b128 v[2:5], v116 offset:4112
	ds_read_b128 v[22:25], v116 offset:8192
	ds_read_b128 v[14:17], v116 offset:8208
	ds_read_b128 v[30:33], v116 offset:12288
	ds_read_b128 v[6:9], v116 offset:12304
	ds_read_b128 v[34:37], v116 offset:16384
	ds_read_b128 v[10:13], v116 offset:16400
	s_waitcnt lgkmcnt(5)
	v_mov_b32_e32 v48, v22
	v_mov_b32_e32 v49, v26
	v_mov_b32_e32 v26, v23
	s_waitcnt lgkmcnt(1)
	v_mov_b32_e32 v46, v34
	v_mov_b32_e32 v47, v30
	v_mov_b32_e32 v30, v35
	v_mov_b32_e32 v52, v24
	v_mov_b32_e32 v53, v28
	v_mov_b32_e32 v28, v25
	v_mov_b32_e32 v50, v36
	v_mov_b32_e32 v51, v32
	v_mov_b32_e32 v32, v37
	ds_read_b128 v[34:37], v116 offset:24592
	ds_read_b128 v[22:25], v116 offset:20496
	v_mov_b32_e32 v80, v38
	v_mov_b32_e32 v81, v18
	v_mov_b32_e32 v18, v39
	v_mov_b32_e32 v82, v40
	v_mov_b32_e32 v83, v20
	v_mov_b32_e32 v20, v41
	ds_read_b128 v[54:57], v116 offset:32768
	ds_read_b128 v[42:45], v116 offset:32784
	ds_read_b128 v[90:93], v116 offset:28672
	ds_read_b128 v[38:41], v116 offset:28688
	v_or_b32_e32 v117, s19, v59
	v_mov_b32_e32 v130, v14
	s_waitcnt lgkmcnt(3)
	v_mov_b32_e32 v94, v54
	s_waitcnt lgkmcnt(1)
	v_mov_b32_e32 v95, v90
	v_mov_b32_e32 v90, v55
	v_mov_b32_e32 v54, v56
	v_mov_b32_e32 v55, v92
	v_mov_b32_e32 v92, v57
	v_mad_i64_i32 v[56:57], s[24:25], v117, s20, v[62:63]
	global_load_dword v72, v[56:57], off nt
	v_or_b32_e32 v56, 1, v117
	v_mad_i64_i32 v[56:57], s[24:25], v56, s20, v[62:63]
	global_load_dword v73, v[56:57], off nt
	v_or_b32_e32 v56, 2, v117
	v_mad_i64_i32 v[56:57], s[24:25], v56, s20, v[62:63]
	global_load_dword v74, v[56:57], off nt
	v_or_b32_e32 v56, 3, v117
	v_mad_i64_i32 v[56:57], s[24:25], v56, s20, v[62:63]
	global_load_dword v75, v[56:57], off nt
	v_or_b32_e32 v56, 4, v117
	v_mad_i64_i32 v[56:57], s[24:25], v56, s20, v[62:63]
	global_load_dword v86, v[56:57], off nt
	v_or_b32_e32 v56, 5, v117
	v_mad_i64_i32 v[56:57], s[24:25], v56, s20, v[62:63]
	global_load_dword v88, v[56:57], off nt
	v_or_b32_e32 v56, 6, v117
	v_mad_i64_i32 v[56:57], s[24:25], v56, s20, v[62:63]
	global_load_dword v96, v[56:57], off nt
	v_or_b32_e32 v56, 7, v117
	v_mad_i64_i32 v[56:57], s[24:25], v56, s20, v[62:63]
	global_load_dword v84, v[56:57], off nt
	v_mov_b32_e32 v131, v2
	v_mov_b32_e32 v2, v15
	v_mov_b32_e32 v132, v16
	v_mov_b32_e32 v133, v4
	v_mov_b32_e32 v4, v17
	v_mov_b32_e32 v138, v10
	v_mov_b32_e32 v139, v6
	v_mov_b32_e32 v6, v11
	v_mov_b32_e32 v140, v12
	v_mov_b32_e32 v141, v8
	v_mov_b32_e32 v8, v13
	v_mov_b32_e32 v146, v34
	v_mov_b32_e32 v147, v22
	v_mov_b32_e32 v22, v35
	v_mov_b32_e32 v148, v36
	v_mov_b32_e32 v149, v24
	v_mov_b32_e32 v24, v37
	v_mov_b32_e32 v154, v42
	s_waitcnt lgkmcnt(0)
	v_mov_b32_e32 v155, v38
	v_mov_b32_e32 v38, v43
	v_mov_b32_e32 v156, v44
	v_mov_b32_e32 v157, v40
	v_mov_b32_e32 v40, v45
	s_mov_b32 s19, 32
	s_waitcnt vmcnt(6)
	v_mov_b32_e32 v56, v73
	v_pk_mul_f32 v[18:19], v[56:57], v[18:19] op_sel_hi:[0,1]
	v_pk_mul_f32 v[26:27], v[56:57], v[26:27] op_sel_hi:[0,1]
	v_pk_fma_f32 v[18:19], v[72:73], v[80:81], v[18:19] op_sel_hi:[0,1,1]
	v_pk_fma_f32 v[26:27], v[72:73], v[48:49], v[26:27] op_sel_hi:[0,1,1]
	s_waitcnt vmcnt(4)
	v_mov_b32_e32 v48, v75
	v_pk_fma_f32 v[18:19], v[74:75], v[82:83], v[18:19] op_sel_hi:[0,1,1]
	v_pk_fma_f32 v[26:27], v[74:75], v[52:53], v[26:27] op_sel_hi:[0,1,1]
	v_pk_fma_f32 v[80:81], v[48:49], v[20:21], v[18:19] op_sel_hi:[0,1,1]
	v_pk_mul_f32 v[18:19], v[56:57], v[90:91] op_sel_hi:[0,1]
	v_pk_fma_f32 v[76:77], v[48:49], v[28:29], v[26:27] op_sel_hi:[0,1,1]
	v_pk_mul_f32 v[26:27], v[56:57], v[30:31] op_sel_hi:[0,1]
	v_pk_fma_f32 v[18:19], v[72:73], v[94:95], v[18:19] op_sel_hi:[0,1,1]
	v_pk_fma_f32 v[26:27], v[72:73], v[46:47], v[26:27] op_sel_hi:[0,1,1]
	v_pk_fma_f32 v[18:19], v[74:75], v[54:55], v[18:19] op_sel_hi:[0,1,1]
	v_pk_fma_f32 v[26:27], v[74:75], v[50:51], v[26:27] op_sel_hi:[0,1,1]
	v_pk_fma_f32 v[82:83], v[48:49], v[92:93], v[18:19] op_sel_hi:[0,1,1]
	ds_read_b128 v[18:21], v116 offset:16
	v_pk_fma_f32 v[78:79], v[48:49], v[32:33], v[26:27] op_sel_hi:[0,1,1]
	ds_read_b128 v[92:95], v116 offset:32
	ds_read_b128 v[30:33], v116 offset:48
	s_waitcnt lgkmcnt(2)
	v_mov_b32_e32 v90, v18
	s_waitcnt lgkmcnt(1)
	v_mov_b32_e32 v91, v92
	v_mov_b32_e32 v92, v19
	v_mov_b32_e32 v110, v20
	v_mov_b32_e32 v111, v94
	v_mov_b32_e32 v94, v21
	ds_read_b128 v[18:21], v116 offset:8224
	ds_read_b128 v[46:49], v116 offset:8240
	ds_read_b128 v[98:101], v116 offset:4128
	ds_read_b128 v[14:17], v116 offset:4144
	s_waitcnt lgkmcnt(3)
	v_mov_b32_e32 v134, v18
	s_waitcnt lgkmcnt(1)
	v_mov_b32_e32 v135, v98
	v_mov_b32_e32 v98, v19
	v_mov_b32_e32 v136, v20
	v_mov_b32_e32 v137, v100
	v_mov_b32_e32 v100, v21
	ds_read_b128 v[18:21], v116 offset:16416
	ds_read_b128 v[50:53], v116 offset:16432
	ds_read_b128 v[118:121], v116 offset:12320
	ds_read_b128 v[10:13], v116 offset:12336
	ds_read_b128 v[26:29], v116 offset:24608
	ds_read_b128 v[34:37], v116 offset:24624
	s_waitcnt lgkmcnt(5)
	v_mov_b32_e32 v142, v18
	s_waitcnt lgkmcnt(3)
	v_mov_b32_e32 v143, v118
	v_mov_b32_e32 v118, v19
	v_mov_b32_e32 v144, v20
	v_mov_b32_e32 v145, v120
	v_mov_b32_e32 v120, v21
	ds_read_b128 v[122:125], v116 offset:20512
	ds_read_b128 v[18:21], v116 offset:20528
	ds_read_b128 v[42:45], v116 offset:32800
	ds_read_b128 v[54:57], v116 offset:32816
	s_waitcnt lgkmcnt(5)
	v_mov_b32_e32 v150, v26
	v_mov_b32_e32 v152, v28
	s_waitcnt lgkmcnt(3)
	v_mov_b32_e32 v151, v122
	v_mov_b32_e32 v122, v27
	v_mov_b32_e32 v153, v124
	v_mov_b32_e32 v124, v29
	ds_read_b128 v[126:129], v116 offset:28704
	ds_read_b128 v[26:29], v116 offset:28720
	s_waitcnt lgkmcnt(3)
; #define LAS __attribute__((address_space(3)))
; __device__ __forceinline__ void p0_phase(Frame& F, KArgs a) {
;     ...
; #pragma unroll 1
;         for (int k0 = 0; k0 < 64; k0 += 32) {
;             float w[32];
; #pragma unroll
;             for (int j = 0; j < 32; ++j) w[j] = wp[(size_t)(kb + k0 + j) * 6144];
; #pragma unroll
;             for (int k = 0; k < 32; k += 4)
; #pragma unroll
;                 for (int s = 0; s < 9; ++s) { const f32x4 sv = *(const LAS f32x4*)(sc + s * 1024 + kb + k0 + k); acc[s] += sv[0] * w[k] + sv[1] * w[k + 1] + sv[2] * w[k + 2] + sv[3] * w[k + 3]; }
;         }
	v_mov_b32_e32 v158, v42
	v_mov_b32_e32 v42, v44
	v_or_b32_e32 v44, 9, v117
	s_waitcnt lgkmcnt(1)
	v_mov_b32_e32 v159, v126
	v_mov_b32_e32 v126, v43
	v_mov_b32_e32 v43, v128
	v_mov_b32_e32 v128, v45
	v_mad_i64_i32 v[44:45], s[24:25], v44, s20, v[62:63]
	global_load_dword v89, v[44:45], off nt
	v_or_b32_e32 v44, 8, v117
	v_mad_i64_i32 v[44:45], s[24:25], v44, s20, v[62:63]
	global_load_dword v87, v[44:45], off nt
	v_or_b32_e32 v44, 10, v117
	v_mad_i64_i32 v[44:45], s[24:25], v44, s20, v[62:63]
	global_load_dword v97, v[44:45], off nt
	v_or_b32_e32 v44, 11, v117
	v_mad_i64_i32 v[44:45], s[24:25], v44, s20, v[62:63]
	global_load_dword v85, v[44:45], off nt
	v_or_b32_e32 v44, 12, v117
	v_mad_i64_i32 v[44:45], s[24:25], v44, s20, v[62:63]
	global_load_dword v106, v[44:45], off nt
	v_or_b32_e32 v44, 13, v117
	v_mad_i64_i32 v[44:45], s[24:25], v44, s20, v[62:63]
	global_load_dword v108, v[44:45], off nt
	v_or_b32_e32 v44, 14, v117
	v_mad_i64_i32 v[44:45], s[24:25], v44, s20, v[62:63]
	global_load_dword v104, v[44:45], off nt
	v_or_b32_e32 v44, 15, v117
	v_mad_i64_i32 v[44:45], s[24:25], v44, s20, v[62:63]
	global_load_dword v102, v[44:45], off nt
	v_mov_b32_e32 v160, v36
	v_mov_b32_e32 v161, v20
	v_mov_b32_e32 v20, v37
	v_mov_b32_e32 v166, v54
	s_waitcnt lgkmcnt(0)
	v_mov_b32_e32 v167, v26
	v_mov_b32_e32 v26, v55
	v_mov_b32_e32 v168, v56
	v_mov_b32_e32 v169, v28
	v_mov_b32_e32 v28, v57
	s_waitcnt vmcnt(7)
	v_pk_mul_f32 v[44:45], v[88:89], v[92:93]
	v_pk_mul_f32 v[2:3], v[88:89], v[2:3] op_sel_hi:[0,1]
	v_pk_mul_f32 v[6:7], v[88:89], v[6:7] op_sel_hi:[0,1]
	v_pk_mul_f32 v[22:23], v[88:89], v[22:23] op_sel_hi:[0,1]
	v_pk_mul_f32 v[38:39], v[88:89], v[38:39] op_sel_hi:[0,1]
	v_mov_b32_e32 v88, v89
	s_waitcnt vmcnt(6)
	v_pk_fma_f32 v[44:45], v[86:87], v[90:91], v[44:45]
	v_pk_fma_f32 v[2:3], v[86:87], v[130:131], v[2:3] op_sel_hi:[0,1,1]
	v_pk_fma_f32 v[6:7], v[86:87], v[138:139], v[6:7] op_sel_hi:[0,1,1]
	v_pk_fma_f32 v[22:23], v[86:87], v[146:147], v[22:23] op_sel_hi:[0,1,1]
	v_pk_fma_f32 v[38:39], v[86:87], v[154:155], v[38:39] op_sel_hi:[0,1,1]
	v_mov_b32_e32 v86, v87
	v_pk_mul_f32 v[90:91], v[88:89], v[98:99] op_sel_hi:[0,1]
	v_pk_fma_f32 v[98:99], v[86:87], v[134:135], v[90:91] op_sel_hi:[0,1,1]
	v_pk_mul_f32 v[90:91], v[88:89], v[118:119] op_sel_hi:[0,1]
	v_pk_fma_f32 v[118:119], v[86:87], v[142:143], v[90:91] op_sel_hi:[0,1,1]
	v_pk_mul_f32 v[90:91], v[88:89], v[122:123] op_sel_hi:[0,1]
	v_pk_mul_f32 v[88:89], v[88:89], v[126:127] op_sel_hi:[0,1]
	s_waitcnt vmcnt(5)
	v_pk_fma_f32 v[2:3], v[96:97], v[132:133], v[2:3] op_sel_hi:[0,1,1]
	v_pk_fma_f32 v[126:127], v[86:87], v[158:159], v[88:89] op_sel_hi:[0,1,1]
	s_waitcnt vmcnt(4)
	v_pk_fma_f32 v[88:89], v[84:85], v[4:5], v[2:3] op_sel_hi:[0,1,1]
	v_pk_fma_f32 v[2:3], v[96:97], v[140:141], v[6:7] op_sel_hi:[0,1,1]
	v_pk_fma_f32 v[122:123], v[86:87], v[150:151], v[90:91] op_sel_hi:[0,1,1]
	v_pk_fma_f32 v[90:91], v[84:85], v[8:9], v[2:3] op_sel_hi:[0,1,1]
	v_pk_fma_f32 v[2:3], v[96:97], v[148:149], v[22:23] op_sel_hi:[0,1,1]
	v_pk_fma_f32 v[44:45], v[96:97], v[110:111], v[44:45]
	v_pk_fma_f32 v[92:93], v[84:85], v[24:25], v[2:3] op_sel_hi:[0,1,1]
	v_pk_fma_f32 v[2:3], v[96:97], v[156:157], v[38:39] op_sel_hi:[0,1,1]
	v_pk_fma_f32 v[86:87], v[84:85], v[94:95], v[44:45]
	v_pk_fma_f32 v[94:95], v[84:85], v[40:41], v[2:3] op_sel_hi:[0,1,1]
	v_mov_b32_e32 v2, v97
	v_pk_fma_f32 v[4:5], v[2:3], v[136:137], v[98:99] op_sel_hi:[0,1,1]
	v_pk_fma_f32 v[6:7], v[2:3], v[144:145], v[118:119] op_sel_hi:[0,1,1]
	v_pk_fma_f32 v[8:9], v[2:3], v[152:153], v[122:123] op_sel_hi:[0,1,1]
	v_pk_fma_f32 v[2:3], v[2:3], v[42:43], v[126:127] op_sel_hi:[0,1,1]
	v_mov_b32_e32 v22, v85
	v_pk_fma_f32 v[96:97], v[22:23], v[100:101], v[4:5] op_sel_hi:[0,1,1]
	v_pk_fma_f32 v[98:99], v[22:23], v[120:121], v[6:7] op_sel_hi:[0,1,1]
	v_pk_fma_f32 v[100:101], v[22:23], v[124:125], v[8:9] op_sel_hi:[0,1,1]
	v_pk_fma_f32 v[84:85], v[22:23], v[128:129], v[2:3] op_sel_hi:[0,1,1]
	ds_read_b128 v[2:5], v116 offset:64
	ds_read_b128 v[38:41], v116 offset:80
	v_mov_b32_e32 v142, v46
	v_mov_b32_e32 v143, v14
	v_mov_b32_e32 v14, v47
	v_mov_b32_e32 v144, v48
	v_mov_b32_e32 v145, v16
	v_mov_b32_e32 v16, v49
	ds_read_b128 v[22:25], v116 offset:8256
	ds_read_b128 v[46:49], v116 offset:8272
	ds_read_b128 v[118:121], v116 offset:4160
	ds_read_b128 v[6:9], v116 offset:4176
	v_mov_b32_e32 v138, v30
	s_waitcnt lgkmcnt(5)
	v_mov_b32_e32 v139, v2
	v_mov_b32_e32 v2, v31
	v_mov_b32_e32 v140, v32
	v_mov_b32_e32 v141, v4
	v_mov_b32_e32 v4, v33
	s_waitcnt lgkmcnt(3)
	v_mov_b32_e32 v146, v22
	s_waitcnt lgkmcnt(1)
	v_mov_b32_e32 v147, v118
	v_mov_b32_e32 v118, v23
	v_mov_b32_e32 v148, v24
	v_mov_b32_e32 v149, v120
	v_mov_b32_e32 v120, v25
	ds_read_b128 v[30:33], v116 offset:16448
	ds_read_b128 v[42:45], v116 offset:16464
	ds_read_b128 v[122:125], v116 offset:12352
	ds_read_b128 v[22:25], v116 offset:12368
	v_mov_b32_e32 v158, v34
	v_mov_b32_e32 v159, v18
	s_waitcnt lgkmcnt(3)
	v_mov_b32_e32 v154, v30
	s_waitcnt lgkmcnt(1)
	v_mov_b32_e32 v155, v122
	v_mov_b32_e32 v122, v31
	v_mov_b32_e32 v156, v32
	v_mov_b32_e32 v157, v124
	v_mov_b32_e32 v124, v33
	v_mov_b32_e32 v18, v35
	ds_read_b128 v[34:37], v116 offset:24640
	ds_read_b128 v[126:129], v116 offset:24656
	ds_read_b128 v[130:133], v116 offset:20544
	ds_read_b128 v[30:33], v116 offset:20560
	v_mov_b32_e32 v150, v50
	v_mov_b32_e32 v151, v10
	v_mov_b32_e32 v10, v51
	v_mov_b32_e32 v152, v52
	v_mov_b32_e32 v153, v12
	v_mov_b32_e32 v12, v53
	ds_read_b128 v[50:53], v116 offset:32832
	ds_read_b128 v[54:57], v116 offset:32848
	s_waitcnt lgkmcnt(5)
	v_mov_b32_e32 v162, v34
	s_waitcnt lgkmcnt(3)
; #define LAS __attribute__((address_space(3)))
; __device__ __forceinline__ void p0_phase(Frame& F, KArgs a) {
;     ...
; #pragma unroll 1
;         for (int k0 = 0; k0 < 64; k0 += 32) {
;             float w[32];
; #pragma unroll
;             for (int j = 0; j < 32; ++j) w[j] = wp[(size_t)(kb + k0 + j) * 6144];
; #pragma unroll
;             for (int k = 0; k < 32; k += 4)
; #pragma unroll
;                 for (int s = 0; s < 9; ++s) { const f32x4 sv = *(const LAS f32x4*)(sc + s * 1024 + kb + k0 + k); acc[s] += sv[0] * w[k] + sv[1] * w[k + 1] + sv[2] * w[k + 2] + sv[3] * w[k + 3]; }
;         }
	v_mov_b32_e32 v163, v130
	v_mov_b32_e32 v130, v35
	v_mov_b32_e32 v164, v36
	v_mov_b32_e32 v165, v132
	v_mov_b32_e32 v132, v37
	ds_read_b128 v[134:137], v116 offset:28736
	ds_read_b128 v[34:37], v116 offset:28752
	s_waitcnt lgkmcnt(3)
	v_mov_b32_e32 v170, v50
	v_mov_b32_e32 v50, v52
	v_or_b32_e32 v52, 17, v117
	s_waitcnt lgkmcnt(1)
	v_mov_b32_e32 v171, v134
	v_mov_b32_e32 v134, v51
	v_mov_b32_e32 v51, v136
	v_mov_b32_e32 v136, v53
	v_mad_i64_i32 v[52:53], s[24:25], v52, s20, v[62:63]
	global_load_dword v109, v[52:53], off nt
	v_or_b32_e32 v52, 16, v117
	v_mad_i64_i32 v[52:53], s[24:25], v52, s20, v[62:63]
	global_load_dword v107, v[52:53], off nt
	v_or_b32_e32 v52, 18, v117
	v_mad_i64_i32 v[52:53], s[24:25], v52, s20, v[62:63]
	global_load_dword v105, v[52:53], off nt
	v_or_b32_e32 v52, 19, v117
	v_mad_i64_i32 v[52:53], s[24:25], v52, s20, v[62:63]
	global_load_dword v103, v[52:53], off nt
	v_or_b32_e32 v52, 20, v117
	v_mad_i64_i32 v[52:53], s[24:25], v52, s20, v[62:63]
	global_load_dword v172, v[52:53], off nt
	v_or_b32_e32 v52, 21, v117
	v_mad_i64_i32 v[52:53], s[24:25], v52, s20, v[62:63]
	global_load_dword v174, v[52:53], off nt
	v_or_b32_e32 v52, 22, v117
	v_mad_i64_i32 v[52:53], s[24:25], v52, s20, v[62:63]
	global_load_dword v110, v[52:53], off nt
	v_or_b32_e32 v52, 23, v117
	v_mad_i64_i32 v[52:53], s[24:25], v52, s20, v[62:63]
	global_load_dword v52, v[52:53], off nt
	v_mov_b32_e32 v178, v126
	v_mov_b32_e32 v179, v30
	v_mov_b32_e32 v30, v127
	v_mov_b32_e32 v180, v128
	v_mov_b32_e32 v181, v32
	v_mov_b32_e32 v32, v129
	v_mov_b32_e32 v186, v54
	s_waitcnt lgkmcnt(0)
	v_mov_b32_e32 v187, v34
	v_mov_b32_e32 v34, v55
	v_mov_b32_e32 v189, v36
	v_mov_b32_e32 v36, v57
	v_or_b32_e32 v57, 31, v117
	v_mov_b32_e32 v188, v56
	s_waitcnt vmcnt(7)
	v_pk_mul_f32 v[2:3], v[108:109], v[2:3]
	v_pk_mul_f32 v[10:11], v[108:109], v[10:11] op_sel_hi:[0,1]
	v_pk_mul_f32 v[14:15], v[108:109], v[14:15] op_sel_hi:[0,1]
	s_waitcnt vmcnt(6)
	v_pk_fma_f32 v[2:3], v[106:107], v[138:139], v[2:3]
	v_pk_fma_f32 v[138:139], v[106:107], v[150:151], v[10:11] op_sel_hi:[0,1,1]
	v_pk_mul_f32 v[10:11], v[108:109], v[18:19] op_sel_hi:[0,1]
	v_pk_fma_f32 v[18:19], v[106:107], v[158:159], v[10:11] op_sel_hi:[0,1,1]
	v_pk_mul_f32 v[10:11], v[108:109], v[26:27] op_sel_hi:[0,1]
	v_pk_fma_f32 v[14:15], v[106:107], v[142:143], v[14:15] op_sel_hi:[0,1,1]
	v_pk_fma_f32 v[26:27], v[106:107], v[166:167], v[10:11] op_sel_hi:[0,1,1]
	v_mov_b32_e32 v106, v109
	v_mov_b32_e32 v10, v107
	v_pk_mul_f32 v[108:109], v[106:107], v[118:119] op_sel_hi:[0,1]
	v_pk_mul_f32 v[118:119], v[106:107], v[122:123] op_sel_hi:[0,1]
	v_pk_mul_f32 v[122:123], v[106:107], v[130:131] op_sel_hi:[0,1]
	v_pk_mul_f32 v[106:107], v[106:107], v[134:135] op_sel_hi:[0,1]
	s_waitcnt vmcnt(5)
	v_pk_fma_f32 v[2:3], v[104:105], v[140:141], v[2:3]
	v_pk_fma_f32 v[108:109], v[10:11], v[146:147], v[108:109] op_sel_hi:[0,1,1]
	v_pk_fma_f32 v[118:119], v[10:11], v[154:155], v[118:119] op_sel_hi:[0,1,1]
	v_pk_fma_f32 v[122:123], v[10:11], v[162:163], v[122:123] op_sel_hi:[0,1,1]
	v_pk_fma_f32 v[106:107], v[10:11], v[170:171], v[106:107] op_sel_hi:[0,1,1]
	s_waitcnt vmcnt(4)
	v_pk_fma_f32 v[10:11], v[102:103], v[4:5], v[2:3]
	v_pk_fma_f32 v[2:3], v[104:105], v[144:145], v[14:15] op_sel_hi:[0,1,1]
	v_pk_fma_f32 v[14:15], v[102:103], v[16:17], v[2:3] op_sel_hi:[0,1,1]
	v_pk_fma_f32 v[2:3], v[104:105], v[152:153], v[138:139] op_sel_hi:[0,1,1]
	v_pk_fma_f32 v[12:13], v[102:103], v[12:13], v[2:3] op_sel_hi:[0,1,1]
	v_pk_fma_f32 v[2:3], v[104:105], v[160:161], v[18:19] op_sel_hi:[0,1,1]
	v_pk_fma_f32 v[16:17], v[102:103], v[20:21], v[2:3] op_sel_hi:[0,1,1]
	v_pk_fma_f32 v[2:3], v[104:105], v[168:169], v[26:27] op_sel_hi:[0,1,1]
	v_pk_fma_f32 v[18:19], v[102:103], v[28:29], v[2:3] op_sel_hi:[0,1,1]
	v_mov_b32_e32 v2, v105
	v_pk_fma_f32 v[4:5], v[2:3], v[148:149], v[108:109] op_sel_hi:[0,1,1]
	v_pk_fma_f32 v[26:27], v[2:3], v[156:157], v[118:119] op_sel_hi:[0,1,1]
	v_pk_fma_f32 v[28:29], v[2:3], v[164:165], v[122:123] op_sel_hi:[0,1,1]
	v_pk_fma_f32 v[2:3], v[2:3], v[50:51], v[106:107] op_sel_hi:[0,1,1]
	v_mov_b32_e32 v50, v103
	v_pk_fma_f32 v[20:21], v[50:51], v[120:121], v[4:5] op_sel_hi:[0,1,1]
	v_pk_fma_f32 v[26:27], v[50:51], v[124:125], v[26:27] op_sel_hi:[0,1,1]
	v_pk_fma_f32 v[28:29], v[50:51], v[132:133], v[28:29] op_sel_hi:[0,1,1]
	v_pk_fma_f32 v[50:51], v[50:51], v[136:137], v[2:3] op_sel_hi:[0,1,1]
	ds_read_b128 v[102:105], v116 offset:96
	ds_read_b128 v[2:5], v116 offset:112
	v_mov_b32_e32 v154, v38
	v_mov_b32_e32 v156, v40
	v_mov_b32_e32 v158, v46
	s_waitcnt lgkmcnt(1)
	v_mov_b32_e32 v155, v102
	v_mov_b32_e32 v102, v39
	v_mov_b32_e32 v157, v104
	v_mov_b32_e32 v104, v41
	v_mov_b32_e32 v159, v6
	v_mov_b32_e32 v6, v47
	v_mov_b32_e32 v160, v48
	v_mov_b32_e32 v161, v8
	v_mov_b32_e32 v8, v49
	ds_read_b128 v[38:41], v116 offset:8288
	ds_read_b128 v[46:49], v116 offset:8304
	ds_read_b128 v[106:109], v116 offset:4192
	ds_read_b128 v[118:121], v116 offset:4208
	v_mov_b32_e32 v166, v42
	v_mov_b32_e32 v167, v22
	s_waitcnt lgkmcnt(3)
	v_mov_b32_e32 v162, v38
	s_waitcnt lgkmcnt(1)
	v_mov_b32_e32 v163, v106
	v_mov_b32_e32 v106, v39
	v_mov_b32_e32 v164, v40
	v_mov_b32_e32 v165, v108
	v_mov_b32_e32 v108, v41
	v_mov_b32_e32 v22, v43
	v_mov_b32_e32 v168, v44
	v_mov_b32_e32 v169, v24
	v_mov_b32_e32 v24, v45
	ds_read_b128 v[38:41], v116 offset:16480
	ds_read_b128 v[122:125], v116 offset:16496
	ds_read_b128 v[42:45], v116 offset:12384
	ds_read_b128 v[130:133], v116 offset:12400
	s_waitcnt lgkmcnt(3)
	v_mov_b32_e32 v170, v38
	s_waitcnt lgkmcnt(1)
; #define LAS __attribute__((address_space(3)))
; __device__ __forceinline__ void p0_phase(Frame& F, KArgs a) {
;     ...
; #pragma unroll 1
;         for (int k0 = 0; k0 < 64; k0 += 32) {
;             float w[32];
; #pragma unroll
;             for (int j = 0; j < 32; ++j) w[j] = wp[(size_t)(kb + k0 + j) * 6144];
; #pragma unroll
;             for (int k = 0; k < 32; k += 4)
; #pragma unroll
;                 for (int s = 0; s < 9; ++s) { const f32x4 sv = *(const LAS f32x4*)(sc + s * 1024 + kb + k0 + k); acc[s] += sv[0] * w[k] + sv[1] * w[k + 1] + sv[2] * w[k + 2] + sv[3] * w[k + 3]; }
;         }
	v_mov_b32_e32 v171, v42
	v_mov_b32_e32 v42, v39
	v_mov_b32_e32 v176, v40
	v_mov_b32_e32 v177, v44
	v_mov_b32_e32 v44, v41
	ds_read_b128 v[38:41], v116 offset:24672
	ds_read_b128 v[126:129], v116 offset:24688
	ds_read_b128 v[134:137], v116 offset:20576
	ds_read_b128 v[138:141], v116 offset:20592
	s_waitcnt lgkmcnt(3)
	v_mov_b32_e32 v182, v38
	s_waitcnt lgkmcnt(1)
	v_mov_b32_e32 v183, v134
	v_mov_b32_e32 v134, v39
	v_mov_b32_e32 v184, v40
	v_mov_b32_e32 v185, v136
	v_mov_b32_e32 v136, v41
	ds_read_b128 v[38:41], v116 offset:32864
	ds_read_b128 v[142:145], v116 offset:32880
	ds_read_b128 v[146:149], v116 offset:28768
	ds_read_b128 v[150:153], v116 offset:28784
	s_waitcnt lgkmcnt(3)
	v_mov_b32_e32 v190, v38
	v_mov_b32_e32 v38, v40
	v_or_b32_e32 v40, 25, v117
	s_waitcnt lgkmcnt(1)
	v_mov_b32_e32 v191, v146
	v_mov_b32_e32 v146, v39
	v_mov_b32_e32 v39, v148
	v_mov_b32_e32 v148, v41
	v_mad_i64_i32 v[40:41], s[24:25], v40, s20, v[62:63]
	global_load_dword v175, v[40:41], off nt
	v_or_b32_e32 v40, 24, v117
	v_mad_i64_i32 v[40:41], s[24:25], v40, s20, v[62:63]
	global_load_dword v173, v[40:41], off nt
	v_or_b32_e32 v40, 26, v117
	v_mad_i64_i32 v[40:41], s[24:25], v40, s20, v[62:63]
	global_load_dword v111, v[40:41], off nt
	v_or_b32_e32 v40, 27, v117
	v_mad_i64_i32 v[40:41], s[24:25], v40, s20, v[62:63]
	global_load_dword v53, v[40:41], off nt
	v_or_b32_e32 v40, 28, v117
	v_mad_i64_i32 v[40:41], s[24:25], v40, s20, v[62:63]
	global_load_dword v54, v[40:41], off nt
	v_or_b32_e32 v40, 29, v117
	v_mad_i64_i32 v[40:41], s[24:25], v40, s20, v[62:63]
	global_load_dword v55, v[40:41], off nt
	v_or_b32_e32 v40, 30, v117
	v_mad_i64_i32 v[40:41], s[24:25], v40, s20, v[62:63]
	global_load_dword v56, v[40:41], off nt
	v_mad_i64_i32 v[40:41], s[24:25], v57, s20, v[62:63]
	global_load_dword v57, v[40:41], off nt
	s_waitcnt vmcnt(7)
	v_pk_mul_f32 v[22:23], v[174:175], v[22:23] op_sel_hi:[0,1]
	v_pk_mul_f32 v[40:41], v[174:175], v[102:103]
	v_pk_mul_f32 v[6:7], v[174:175], v[6:7] op_sel_hi:[0,1]
	s_waitcnt vmcnt(6)
	v_pk_fma_f32 v[102:103], v[172:173], v[166:167], v[22:23] op_sel_hi:[0,1,1]
	v_pk_mul_f32 v[22:23], v[174:175], v[30:31] op_sel_hi:[0,1]
	v_pk_fma_f32 v[40:41], v[172:173], v[154:155], v[40:41]
	v_pk_fma_f32 v[6:7], v[172:173], v[158:159], v[6:7] op_sel_hi:[0,1,1]
	v_pk_fma_f32 v[154:155], v[172:173], v[178:179], v[22:23] op_sel_hi:[0,1,1]
	v_pk_mul_f32 v[22:23], v[174:175], v[34:35] op_sel_hi:[0,1]
	v_mov_b32_e32 v30, v175
	v_pk_fma_f32 v[34:35], v[172:173], v[186:187], v[22:23] op_sel_hi:[0,1,1]
	v_mov_b32_e32 v22, v173
	v_pk_mul_f32 v[106:107], v[30:31], v[106:107] op_sel_hi:[0,1]
	v_pk_mul_f32 v[42:43], v[30:31], v[42:43] op_sel_hi:[0,1]
	v_pk_mul_f32 v[134:135], v[30:31], v[134:135] op_sel_hi:[0,1]
	v_pk_mul_f32 v[30:31], v[30:31], v[146:147] op_sel_hi:[0,1]
	s_waitcnt vmcnt(5)
	v_pk_fma_f32 v[6:7], v[110:111], v[160:161], v[6:7] op_sel_hi:[0,1,1]
	v_pk_fma_f32 v[146:147], v[22:23], v[190:191], v[30:31] op_sel_hi:[0,1,1]
	s_waitcnt vmcnt(4)
	v_pk_fma_f32 v[30:31], v[52:53], v[8:9], v[6:7] op_sel_hi:[0,1,1]
	v_pk_fma_f32 v[6:7], v[110:111], v[168:169], v[102:103] op_sel_hi:[0,1,1]
	v_pk_fma_f32 v[24:25], v[52:53], v[24:25], v[6:7] op_sel_hi:[0,1,1]
	v_pk_fma_f32 v[6:7], v[110:111], v[180:181], v[154:155] op_sel_hi:[0,1,1]
	v_pk_fma_f32 v[32:33], v[52:53], v[32:33], v[6:7] op_sel_hi:[0,1,1]
	v_pk_fma_f32 v[6:7], v[110:111], v[188:189], v[34:35] op_sel_hi:[0,1,1]
	v_pk_fma_f32 v[106:107], v[22:23], v[162:163], v[106:107] op_sel_hi:[0,1,1]
	v_pk_fma_f32 v[42:43], v[22:23], v[170:171], v[42:43] op_sel_hi:[0,1,1]
	v_pk_fma_f32 v[134:135], v[22:23], v[182:183], v[134:135] op_sel_hi:[0,1,1]
	v_pk_fma_f32 v[22:23], v[110:111], v[156:157], v[40:41]
	v_pk_fma_f32 v[34:35], v[52:53], v[36:37], v[6:7] op_sel_hi:[0,1,1]
	v_mov_b32_e32 v6, v111
	v_pk_fma_f32 v[22:23], v[52:53], v[104:105], v[22:23]
	v_pk_fma_f32 v[8:9], v[6:7], v[164:165], v[106:107] op_sel_hi:[0,1,1]
	v_pk_fma_f32 v[40:41], v[6:7], v[176:177], v[42:43] op_sel_hi:[0,1,1]
	v_pk_fma_f32 v[42:43], v[6:7], v[184:185], v[134:135] op_sel_hi:[0,1,1]
	v_pk_fma_f32 v[6:7], v[6:7], v[38:39], v[146:147] op_sel_hi:[0,1,1]
	v_mov_b32_e32 v52, v53
	v_pk_fma_f32 v[36:37], v[52:53], v[108:109], v[8:9] op_sel_hi:[0,1,1]
	v_pk_fma_f32 v[38:39], v[52:53], v[44:45], v[40:41] op_sel_hi:[0,1,1]
	v_pk_fma_f32 v[40:41], v[52:53], v[136:137], v[42:43] op_sel_hi:[0,1,1]
	v_pk_fma_f32 v[42:43], v[52:53], v[148:149], v[6:7] op_sel_hi:[0,1,1]
	v_mov_b32_e32 v7, v118
	v_mov_b32_e32 v118, v47
	s_waitcnt vmcnt(2)
	v_mov_b32_e32 v108, v55
	v_mov_b32_e32 v6, v46
	v_pk_mul_f32 v[44:45], v[108:109], v[118:119] op_sel_hi:[0,1]
	v_mov_b32_e32 v8, v48
	v_mov_b32_e32 v9, v120
	v_pk_fma_f32 v[6:7], v[54:55], v[6:7], v[44:45] op_sel_hi:[0,1,1]
	v_mov_b32_e32 v120, v49
	v_mov_b32_e32 v47, v130
	v_mov_b32_e32 v130, v123
	s_waitcnt vmcnt(0)
	v_pk_fma_f32 v[6:7], v[56:57], v[8:9], v[6:7] op_sel_hi:[0,1,1]
	v_mov_b32_e32 v8, v57
	v_mov_b32_e32 v46, v122
	v_pk_fma_f32 v[44:45], v[8:9], v[120:121], v[6:7] op_sel_hi:[0,1,1]
	v_pk_mul_f32 v[6:7], v[108:109], v[130:131] op_sel_hi:[0,1]
	v_mov_b32_e32 v48, v124
	v_mov_b32_e32 v49, v132
	v_pk_fma_f32 v[6:7], v[54:55], v[46:47], v[6:7] op_sel_hi:[0,1,1]
	v_mov_b32_e32 v132, v125
	v_mov_b32_e32 v53, v138
	v_mov_b32_e32 v138, v127
	v_pk_fma_f32 v[6:7], v[56:57], v[48:49], v[6:7] op_sel_hi:[0,1,1]
	v_mov_b32_e32 v52, v126
	v_pk_fma_f32 v[46:47], v[8:9], v[132:133], v[6:7] op_sel_hi:[0,1,1]
	v_pk_mul_f32 v[6:7], v[108:109], v[138:139] op_sel_hi:[0,1]
	v_mov_b32_e32 v102, v128
	v_mov_b32_e32 v103, v140
	v_pk_fma_f32 v[6:7], v[54:55], v[52:53], v[6:7] op_sel_hi:[0,1,1]
	v_mov_b32_e32 v140, v129
	s_waitcnt lgkmcnt(0)
; #define LAS __attribute__((address_space(3)))
; __device__ __forceinline__ const float* IN(KArgs a, int i) { return (const float*)a->in[i]; }
; #define a launder(kargs)
; __device__ __forceinline__ void p0_phase(Frame& F, KArgs a) {
;     ...
;             for (int k = 0; k < 32; k += 4)
; #pragma unroll
;                 for (int s = 0; s < 9; ++s) { const f32x4 sv = *(const LAS f32x4*)(sc + s * 1024 + kb + k0 + k); acc[s] += sv[0] * w[k] + sv[1] * w[k + 1] + sv[2] * w[k + 2] + sv[3] * w[k + 3]; }
;         }
; #pragma unroll
;         for (int s = 0; s < 9; ++s) part[(F.wave * 9 + s) * 64 + F.lane] = acc[s];
;         __syncthreads();
;         for (int i = F.tid; i < 9 * 32; i += 512) { const int s = i >> 5, l = i & 31; float v = 0.f;
; #pragma unroll
;             for (int w = 0; w < 8; ++w) v += part[(w * 9 + s) * 64 + l] + part[(w * 9 + s) * 64 + 32 + l];
;             const int cc = cb * 32 + l;
;             MOD[((size_t)(L * 9 + s) * 6) * 1024 + cc] = v + IN(a, I_BADA)[L * 6144 + cc]; }
	v_mov_b32_e32 v105, v150
	v_mov_b32_e32 v150, v143
	v_pk_fma_f32 v[6:7], v[56:57], v[102:103], v[6:7] op_sel_hi:[0,1,1]
	v_mov_b32_e32 v104, v142
	v_pk_fma_f32 v[48:49], v[8:9], v[140:141], v[6:7] op_sel_hi:[0,1,1]
	v_pk_mul_f32 v[6:7], v[108:109], v[150:151] op_sel_hi:[0,1]
	v_mov_b32_e32 v106, v144
	v_mov_b32_e32 v107, v152
	v_pk_fma_f32 v[6:7], v[54:55], v[104:105], v[6:7] op_sel_hi:[0,1,1]
	v_mov_b32_e32 v152, v145
	v_pk_fma_f32 v[6:7], v[56:57], v[106:107], v[6:7] op_sel_hi:[0,1,1]
	v_pk_fma_f32 v[52:53], v[8:9], v[152:153], v[6:7] op_sel_hi:[0,1,1]
	ds_read_b128 v[6:9], v116
	v_pk_mul_f32 v[2:3], v[54:55], v[2:3]
	v_pk_mul_f32 v[4:5], v[56:57], v[4:5]
	v_add_f32_e32 v2, v2, v3
	v_add_f32_e32 v2, v4, v2
	s_waitcnt lgkmcnt(0)
	v_pk_mul_f32 v[6:7], v[72:73], v[6:7]
	v_pk_mul_f32 v[8:9], v[74:75], v[8:9]
	v_add_f32_e32 v6, v6, v7
	v_add_f32_e32 v6, v8, v6
	v_add_f32_e32 v54, v9, v6
	v_add_f32_e32 v55, v5, v2
	v_pk_add_f32 v[2:3], v[70:71], v[76:77]
	v_pk_add_f32 v[4:5], v[68:69], v[78:79]
	v_pk_add_f32 v[6:7], v[66:67], v[80:81]
	v_pk_add_f32 v[8:9], v[64:65], v[82:83]
	v_add_f32_e32 v54, v115, v54
	v_add_f32_e32 v54, v54, v86
	v_pk_add_f32 v[2:3], v[2:3], v[88:89]
	v_pk_add_f32 v[4:5], v[4:5], v[90:91]
	v_pk_add_f32 v[6:7], v[6:7], v[92:93]
	v_pk_add_f32 v[8:9], v[8:9], v[94:95]
	v_add_f32_e32 v54, v54, v87
	v_pk_add_f32 v[2:3], v[2:3], v[96:97]
	v_pk_add_f32 v[4:5], v[4:5], v[98:99]
	v_pk_add_f32 v[6:7], v[6:7], v[100:101]
	v_pk_add_f32 v[8:9], v[8:9], v[84:85]
	v_add_f32_e32 v10, v54, v10
	v_pk_add_f32 v[2:3], v[2:3], v[14:15]
	v_pk_add_f32 v[4:5], v[4:5], v[12:13]
	v_pk_add_f32 v[6:7], v[6:7], v[16:17]
	v_pk_add_f32 v[8:9], v[8:9], v[18:19]
	v_add_f32_e32 v10, v10, v11
	v_pk_add_f32 v[2:3], v[2:3], v[20:21]
	v_pk_add_f32 v[4:5], v[4:5], v[26:27]
	v_pk_add_f32 v[6:7], v[6:7], v[28:29]
	v_pk_add_f32 v[8:9], v[8:9], v[50:51]
	v_cndmask_b32_e64 v56, 0, 1, s[10:11]
	v_add_f32_e32 v10, v10, v22
	v_pk_add_f32 v[2:3], v[2:3], v[30:31]
	v_pk_add_f32 v[4:5], v[4:5], v[24:25]
	v_pk_add_f32 v[6:7], v[6:7], v[32:33]
	v_pk_add_f32 v[8:9], v[8:9], v[34:35]
	v_cmp_ne_u32_e32 vcc, 1, v56
	v_add_f32_e32 v10, v10, v23
	v_pk_add_f32 v[2:3], v[2:3], v[36:37]
	v_pk_add_f32 v[4:5], v[4:5], v[38:39]
	v_pk_add_f32 v[6:7], v[6:7], v[40:41]
	v_pk_add_f32 v[8:9], v[8:9], v[42:43]
	s_mov_b64 s[10:11], 0
	s_and_b64 vcc, exec, vcc
	v_add_f32_e32 v115, v10, v55
	v_pk_add_f32 v[70:71], v[2:3], v[44:45]
	v_pk_add_f32 v[68:69], v[4:5], v[46:47]
	v_pk_add_f32 v[66:67], v[6:7], v[48:49]
	v_pk_add_f32 v[64:65], v[8:9], v[52:53]
	s_cbranch_vccz .LBB0_24
	ds_write2st64_b32 v114, v115, v71 offset0:160 offset1:161
	ds_write2st64_b32 v114, v70, v69 offset0:162 offset1:163
	ds_write2st64_b32 v114, v68, v67 offset0:164 offset1:165
	ds_write2st64_b32 v114, v66, v65 offset0:166 offset1:167
	ds_write_b32 v114, v64 offset:43008
	s_waitcnt lgkmcnt(0)
	s_barrier
	s_and_saveexec_b64 s[10:11], s[4:5]
	s_cbranch_execz .LBB0_22
	s_load_dwordx2 s[24:25], s[14:15], 0x28
	s_mul_i32 s19, s18, 0x1800
	v_add_u32_e32 v2, s19, v60
	v_ashrrev_i32_e32 v3, 31, v2
	s_mul_i32 s23, s18, 9
	s_waitcnt lgkmcnt(0)
	v_lshl_add_u64 v[2:3], v[2:3], 2, s[24:25]
	v_lshl_add_u64 v[4:5], v[60:61], 2, s[6:7]
	s_mov_b64 s[18:19], 0
	v_mov_b32_e32 v6, v202
.LBB0_27:
	global_load_dword v7, v[2:3], off nt
	v_ashrrev_i32_e32 v8, 5, v6
	v_lshl_add_u32 v10, v8, 8, v113
	v_add_u32_e32 v11, 0xa000, v10
	v_add_u32_e32 v12, 0xa800, v10
	v_add_u32_e32 v14, 0xb000, v10
	v_add_u32_e32 v16, 0xb800, v10
	v_add_u32_e32 v18, 0xc400, v10
	v_add_u32_e32 v20, 0xcc00, v10
	v_add_u32_e32 v22, 0xd400, v10
	v_add_u32_e32 v24, 0xdc00, v10
	ds_read2_b32 v[10:11], v11 offset1:32
	ds_read2_b32 v[12:13], v12 offset0:64 offset1:96
	ds_read2_b32 v[14:15], v14 offset0:128 offset1:160
	ds_read2_b32 v[16:17], v16 offset0:192 offset1:224
	ds_read2_b32 v[18:19], v18 offset1:32
	ds_read2_b32 v[20:21], v20 offset0:64 offset1:96
	ds_read2_b32 v[22:23], v22 offset0:128 offset1:160
	ds_read2_b32 v[24:25], v24 offset0:192 offset1:224
	s_waitcnt lgkmcnt(7)
	v_mov_b32_e32 v26, v10
	s_waitcnt lgkmcnt(6)
	v_mov_b32_e32 v27, v12
	v_mov_b32_e32 v12, v11
	v_pk_add_f32 v[12:13], v[26:27], v[12:13]
	s_waitcnt lgkmcnt(5)
	v_mov_b32_e32 v10, v14
	s_waitcnt lgkmcnt(4)
	v_mov_b32_e32 v11, v16
	v_mov_b32_e32 v16, v15
	v_add_f32_e32 v12, 0, v12
	v_pk_add_f32 v[10:11], v[10:11], v[16:17]
	v_add_f32_e32 v12, v12, v13
	s_waitcnt lgkmcnt(3)
	v_mov_b32_e32 v14, v18
	s_waitcnt lgkmcnt(2)
	v_mov_b32_e32 v15, v20
	v_mov_b32_e32 v20, v19
	v_add_f32_e32 v10, v12, v10
	v_pk_add_f32 v[14:15], v[14:15], v[20:21]
	v_add_f32_e32 v10, v10, v11
	s_waitcnt lgkmcnt(1)
	v_mov_b32_e32 v18, v22
	s_waitcnt lgkmcnt(0)
	v_mov_b32_e32 v19, v24
	v_mov_b32_e32 v24, v23
	v_add_f32_e32 v10, v10, v14
	v_pk_add_f32 v[16:17], v[18:19], v[24:25]
	v_add_f32_e32 v10, v10, v15
	v_add_f32_e32 v10, v10, v16
	v_add_u32_e32 v9, 0x200, v6
	v_cmp_lt_i32_e32 vcc, s21, v6
	v_add_u32_e32 v8, s23, v8
	v_add_f32_e32 v10, v10, v17
	s_or_b64 s[18:19], vcc, s[18:19]
	v_mov_b32_e32 v6, v9
	v_mad_i64_i32 v[8:9], s[24:25], v8, s20, v[4:5]
	s_waitcnt vmcnt(0)
	v_add_f32_e32 v7, v7, v10
	global_store_dword v[8:9], v7, off
	s_andn2_b64 exec, exec, s[18:19]
	s_cbranch_execnz .LBB0_27
	s_branch .LBB0_22

; #define LDS_WAIT() asm volatile("s_waitcnt lgkmcnt(0)" ::: "memory")
; __device__ __forceinline__ void transpose_item(const float* W, int ldw, int k0, int n0, bf16_t* dstrow0, int ldt, LAS float* scr, int lane) {
;     ...
;     for (int i = 0; i < 32; ++i) { const int kk = 2 * i + (lane >> 5); scr[kk * 33 + (lane & 31)] = W[(size_t)(k0 + kk) * ldw + n0 + (lane & 31)]; }
;     LDS_WAIT(); asm volatile("" ::: "memory");
.LBB0_70:
	s_lshl_b32 s25, s19, 1
	s_lshl_b32 s39, s22, 1
	v_or_b32_e32 v25, s39, v2
	s_add_i32 s40, s25, 4
	s_add_i32 s41, s39, 4
	s_add_i32 s43, s39, 8
	v_add_u32_e32 v4, s18, v25
	v_or_b32_e32 v27, s40, v1
	v_or_b32_e32 v52, s41, v2
	v_mov_b32_e32 v33, v5
	v_or_b32_e32 v7, s25, v1
	s_add_i32 s45, s39, 12
	v_or_b32_e32 v54, s43, v2
	v_lshlrev_b64 v[46:47], 12, v[4:5]
	v_add_u32_e32 v32, s21, v27
	v_add_u32_e32 v4, s18, v52
	v_mov_b32_e32 v31, v5
	s_add_i32 s42, s25, 8
	s_add_i32 s44, s25, 12
	s_add_i32 s47, s39, 16
	v_add_u32_e32 v30, s21, v7
	v_or_b32_e32 v56, s45, v2
	v_lshlrev_b64 v[32:33], 12, v[32:33]
	v_lshlrev_b64 v[48:49], 12, v[4:5]
	v_add_u32_e32 v4, s18, v54
	s_add_i32 s49, s39, 20
	v_or_b32_e32 v53, s42, v1
	v_or_b32_e32 v55, s44, v1
	v_or_b32_e32 v58, s47, v2
	v_lshlrev_b64 v[30:31], 12, v[30:31]
	v_lshl_add_u64 v[46:47], v[28:29], 0, v[46:47]
	v_lshl_add_u64 v[32:33], v[28:29], 0, v[32:33]
	v_lshlrev_b64 v[50:51], 12, v[4:5]
	v_add_u32_e32 v4, s18, v56
	v_mov_b32_e32 v35, v5
	v_mov_b32_e32 v37, v5
	s_add_i32 s46, s25, 16
	s_add_i32 s48, s25, 20
	s_add_i32 s51, s39, 24
	v_or_b32_e32 v60, s49, v2
	v_add_u32_e32 v34, s21, v53
	v_add_u32_e32 v36, s21, v55
	v_lshl_add_u64 v[30:31], v[28:29], 0, v[30:31]
	v_lshl_add_u64 v[48:49], v[28:29], 0, v[48:49]
	global_load_dword v65, v[46:47], off nt
	global_load_dword v66, v[30:31], off nt
	global_load_dword v67, v[48:49], off nt
	global_load_dword v68, v[32:33], off nt
	v_lshlrev_b64 v[32:33], 12, v[4:5]
	v_add_u32_e32 v4, s18, v58
	s_add_i32 s50, s25, 24
	s_add_i32 s25, s25, 28
	s_add_i32 s39, s39, 28
	v_or_b32_e32 v57, s46, v1
	v_or_b32_e32 v59, s48, v1
	v_or_b32_e32 v62, s51, v2
	v_lshlrev_b64 v[34:35], 12, v[34:35]
	v_lshlrev_b64 v[36:37], 12, v[36:37]
	v_lshl_add_u64 v[30:31], v[28:29], 0, v[50:51]
	v_lshl_add_u64 v[32:33], v[28:29], 0, v[32:33]
	v_lshlrev_b64 v[46:47], 12, v[4:5]
	v_add_u32_e32 v4, s18, v60
	v_mov_b32_e32 v39, v5
	v_mov_b32_e32 v41, v5
	v_or_b32_e32 v61, s50, v1
	v_or_b32_e32 v63, s25, v1
	v_or_b32_e32 v64, s39, v2
	v_add_u32_e32 v38, s21, v57
	v_add_u32_e32 v40, s21, v59
	v_lshl_add_u64 v[34:35], v[28:29], 0, v[34:35]
	v_lshl_add_u64 v[36:37], v[28:29], 0, v[36:37]
	global_load_dword v69, v[30:31], off nt
	global_load_dword v70, v[34:35], off nt
	global_load_dword v71, v[32:33], off nt
	global_load_dword v72, v[36:37], off nt
	v_lshlrev_b64 v[32:33], 12, v[4:5]
	v_add_u32_e32 v4, s18, v62
	v_mov_b32_e32 v43, v5
	v_mov_b32_e32 v45, v5
	v_add_u32_e32 v42, s21, v61
	v_add_u32_e32 v44, s21, v63
	v_lshlrev_b64 v[38:39], 12, v[38:39]
	v_lshlrev_b64 v[40:41], 12, v[40:41]
	v_lshl_add_u64 v[30:31], v[28:29], 0, v[46:47]
	v_lshl_add_u64 v[32:33], v[28:29], 0, v[32:33]
	v_lshlrev_b64 v[34:35], 12, v[4:5]
	v_add_u32_e32 v4, s18, v64
	v_lshlrev_b64 v[42:43], 12, v[42:43]
	v_lshlrev_b64 v[44:45], 12, v[44:45]
	v_lshl_add_u64 v[38:39], v[28:29], 0, v[38:39]
	v_lshl_add_u64 v[40:41], v[28:29], 0, v[40:41]
	global_load_dword v73, v[30:31], off nt
	global_load_dword v74, v[38:39], off nt
	global_load_dword v75, v[32:33], off nt
	global_load_dword v76, v[40:41], off nt
	v_lshl_add_u64 v[30:31], v[28:29], 0, v[34:35]
	v_lshlrev_b64 v[32:33], 12, v[4:5]
	v_lshl_add_u64 v[42:43], v[28:29], 0, v[42:43]
	v_lshl_add_u64 v[44:45], v[28:29], 0, v[44:45]
	v_lshl_add_u64 v[32:33], v[28:29], 0, v[32:33]
	global_load_dword v4, v[30:31], off nt
	global_load_dword v77, v[42:43], off nt
	global_load_dword v78, v[32:33], off nt
	global_load_dword v79, v[44:45], off nt
	s_add_i32 s22, s22, 16
	s_add_i32 s19, s19, 16
	s_add_i32 s23, s23, -16
	v_mad_u64_u32 v[30:31], s[40:41], v25, s35, v[6:7]
	s_cmp_lg_u32 s23, 0
	v_mad_u64_u32 v[32:33], s[40:41], v7, s35, v[6:7]
	v_mad_u64_u32 v[34:35], s[40:41], v52, s35, v[6:7]
	v_mad_u64_u32 v[36:37], s[40:41], v27, s35, v[6:7]
	v_mad_u64_u32 v[38:39], s[40:41], v54, s35, v[6:7]
	v_mad_u64_u32 v[40:41], s[40:41], v53, s35, v[6:7]
	v_mad_u64_u32 v[42:43], s[40:41], v56, s35, v[6:7]
	v_mad_u64_u32 v[44:45], s[40:41], v55, s35, v[6:7]
	v_mad_u64_u32 v[46:47], s[40:41], v58, s35, v[6:7]
	v_mad_u64_u32 v[48:49], s[40:41], v57, s35, v[6:7]
	v_mad_u64_u32 v[50:51], s[40:41], v60, s35, v[6:7]
	v_mad_u64_u32 v[52:53], s[40:41], v59, s35, v[6:7]
	v_mad_u64_u32 v[54:55], s[40:41], v62, s35, v[6:7]
	v_mad_u64_u32 v[56:57], s[40:41], v61, s35, v[6:7]
	v_mad_u64_u32 v[58:59], s[40:41], v64, s35, v[6:7]
	v_mad_u64_u32 v[60:61], s[40:41], v63, s35, v[6:7]
	s_waitcnt vmcnt(15)
	ds_write_b32 v30, v65 offset:61440
	s_waitcnt vmcnt(14)
	ds_write_b32 v32, v66 offset:61440
	s_waitcnt vmcnt(13)
	ds_write_b32 v34, v67 offset:61440
	s_waitcnt vmcnt(12)
	ds_write_b32 v36, v68 offset:61440
	s_waitcnt vmcnt(11)
	ds_write_b32 v38, v69 offset:61440
	s_waitcnt vmcnt(10)
	ds_write_b32 v40, v70 offset:61440
	s_waitcnt vmcnt(9)
	ds_write_b32 v42, v71 offset:61440
	s_waitcnt vmcnt(8)
	ds_write_b32 v44, v72 offset:61440
	s_waitcnt vmcnt(7)
	ds_write_b32 v46, v73 offset:61440
	s_waitcnt vmcnt(6)
	ds_write_b32 v48, v74 offset:61440
	s_waitcnt vmcnt(5)
	ds_write_b32 v50, v75 offset:61440
	s_waitcnt vmcnt(4)
	ds_write_b32 v52, v76 offset:61440
	s_waitcnt vmcnt(3)
	ds_write_b32 v54, v4 offset:61440
	s_waitcnt vmcnt(2)
	ds_write_b32 v56, v77 offset:61440
	s_waitcnt vmcnt(1)
	ds_write_b32 v58, v78 offset:61440
	s_waitcnt vmcnt(0)
	ds_write_b32 v60, v79 offset:61440
	s_cbranch_scc1 .LBB0_70
; #define LAS __attribute__((address_space(3)))
; __device__ __forceinline__ unsigned cvtpk(float lo, float hi) { f32x2 v = {lo, hi}; bf16x2_t b = __builtin_convertvector(v, bf16x2_t); return __builtin_bit_cast(unsigned, b); }
; #define LDS_WAIT() asm volatile("s_waitcnt lgkmcnt(0)" ::: "memory")
; __device__ __forceinline__ void transpose_item(const float* W, int ldw, int k0, int n0, bf16_t* dstrow0, int ldt, LAS float* scr, int lane) {
;     ...
;     const int c = lane & 7;
; #pragma unroll
;     for (int j = 0; j < 4; ++j) { const int n = (lane >> 3) + 8 * j; const LAS float* s = scr + (8 * c) * 33 + n;
;         u32x4 o; o.x = cvtpk(s[0 * 33], s[1 * 33]); o.y = cvtpk(s[2 * 33], s[3 * 33]); o.z = cvtpk(s[4 * 33], s[5 * 33]); o.w = cvtpk(s[6 * 33], s[7 * 33]);
;         *(u32x4*)(dstrow0 + (size_t)n * ldt + k0 + 8 * c) = o; }
;     LDS_WAIT(); asm volatile("" ::: "memory");
	s_lshl_b64 s[22:23], s[4:5], 21
	s_add_u32 s5, s28, s22
	s_waitcnt lgkmcnt(0)
	s_addc_u32 s19, s29, s23
	s_lshl_b32 s20, s20, 11
	s_add_u32 s5, s5, s20
	ds_read2_b32 v[32:33], v3 offset0:33 offset1:41
	ds_read2_b32 v[34:35], v3 offset1:8
	ds_read2_b32 v[36:37], v3 offset0:66 offset1:74
	ds_read2_b32 v[38:39], v3 offset0:99 offset1:107
	ds_read2_b32 v[40:41], v3 offset0:132 offset1:140
	ds_read2_b32 v[42:43], v3 offset0:165 offset1:173
	ds_read2_b32 v[44:45], v3 offset0:198 offset1:206
	ds_read2_b32 v[46:47], v3 offset0:231 offset1:239
	s_addc_u32 s19, s19, 0
	s_lshl_b32 s18, s18, 1
	s_add_u32 s18, s5, s18
	s_addc_u32 s19, s19, 0
	v_mov_b32_e32 v27, v5
	v_lshl_add_u64 v[48:49], s[18:19], 0, v[26:27]
	s_waitcnt lgkmcnt(6)
	v_cvt_pk_bf16_f32 v28, v34, v32
	s_waitcnt lgkmcnt(4)
	v_cvt_pk_bf16_f32 v29, v36, v38
	s_waitcnt lgkmcnt(2)
	v_cvt_pk_bf16_f32 v30, v40, v42
	s_waitcnt lgkmcnt(0)
	v_cvt_pk_bf16_f32 v31, v44, v46
	v_lshl_add_u64 v[50:51], v[48:49], 0, v[8:9]
	global_store_dwordx4 v[50:51], v[28:31], off
	s_mov_b64 s[18:19], 0
	s_nop 0
	v_cvt_pk_bf16_f32 v28, v35, v33
	v_cvt_pk_bf16_f32 v29, v37, v39
	v_cvt_pk_bf16_f32 v30, v41, v43
	v_cvt_pk_bf16_f32 v31, v45, v47
	ds_read2_b32 v[34:35], v3 offset0:49 offset1:57
	ds_read2_b32 v[36:37], v3 offset0:16 offset1:24
	ds_read2_b32 v[38:39], v3 offset0:82 offset1:90
	ds_read2_b32 v[40:41], v3 offset0:115 offset1:123
	ds_read2_b32 v[42:43], v3 offset0:148 offset1:156
	ds_read2_b32 v[44:45], v3 offset0:181 offset1:189
	ds_read2_b32 v[46:47], v3 offset0:214 offset1:222
	ds_read2_b32 v[50:51], v3 offset0:247 offset1:255
	v_lshl_add_u64 v[32:33], v[48:49], 0, v[10:11]
	global_store_dwordx4 v[32:33], v[28:31], off
	v_lshl_add_u64 v[32:33], v[48:49], 0, v[12:13]
	s_waitcnt lgkmcnt(6)
	v_cvt_pk_bf16_f32 v28, v36, v34
	s_waitcnt lgkmcnt(4)
	v_cvt_pk_bf16_f32 v29, v38, v40
	s_waitcnt lgkmcnt(2)
	v_cvt_pk_bf16_f32 v30, v42, v44
	s_waitcnt lgkmcnt(0)
	v_cvt_pk_bf16_f32 v31, v46, v50
	global_store_dwordx4 v[32:33], v[28:31], off
	v_lshl_add_u64 v[32:33], v[48:49], 0, v[14:15]
	s_nop 0
	v_cvt_pk_bf16_f32 v28, v37, v35
	v_cvt_pk_bf16_f32 v29, v39, v41
	v_cvt_pk_bf16_f32 v30, v43, v45
	v_cvt_pk_bf16_f32 v31, v47, v51
	global_store_dwordx4 v[32:33], v[28:31], off
	s_waitcnt lgkmcnt(0)

; #define LDS_WAIT() asm volatile("s_waitcnt lgkmcnt(0)" ::: "memory")
; __device__ __forceinline__ void transpose_item(const float* W, int ldw, int k0, int n0, bf16_t* dstrow0, int ldt, LAS float* scr, int lane) {
;     ...
;     for (int i = 0; i < 32; ++i) { const int kk = 2 * i + (lane >> 5); scr[kk * 33 + (lane & 31)] = W[(size_t)(k0 + kk) * ldw + n0 + (lane & 31)]; }
;     LDS_WAIT(); asm volatile("" ::: "memory");
.LBB0_78:
	s_lshl_b32 s40, s23, 1
	s_lshl_b32 s41, s25, 1
	v_or_b32_e32 v4, s40, v1
	v_or_b32_e32 v7, s41, v2
	s_add_i32 s42, s40, 4
	s_add_i32 s43, s41, 4
	s_add_i32 s44, s40, 8
	s_add_i32 s45, s41, 8
	s_add_i32 s46, s40, 12
	s_add_i32 s47, s41, 12
	s_add_i32 s48, s40, 16
	s_add_i32 s49, s41, 16
	s_add_i32 s50, s40, 20
	s_add_i32 s51, s41, 20
	s_add_i32 s52, s40, 24
	s_add_i32 s53, s41, 24
	s_add_i32 s40, s40, 28
	s_add_i32 s41, s41, 28
	v_add_u32_e32 v32, s22, v7
	v_or_b32_e32 v25, s42, v1
	v_or_b32_e32 v27, s43, v2
	v_or_b32_e32 v62, s44, v1
	v_or_b32_e32 v63, s45, v2
	v_or_b32_e32 v64, s46, v1
	v_or_b32_e32 v65, s47, v2
	v_or_b32_e32 v66, s48, v1
	v_or_b32_e32 v67, s49, v2
	v_or_b32_e32 v68, s50, v1
	v_or_b32_e32 v69, s51, v2
	v_or_b32_e32 v70, s52, v1
	v_or_b32_e32 v71, s53, v2
	v_or_b32_e32 v72, s40, v1
	v_or_b32_e32 v73, s41, v2
	v_add_u32_e32 v30, s5, v4
	v_ashrrev_i32_e32 v33, 31, v32
	v_add_u32_e32 v34, s5, v25
	v_add_u32_e32 v36, s22, v27
	v_add_u32_e32 v38, s5, v62
	v_add_u32_e32 v40, s22, v63
	v_add_u32_e32 v42, s5, v64
	v_add_u32_e32 v44, s22, v65
	v_add_u32_e32 v46, s5, v66
	v_add_u32_e32 v48, s22, v67
	v_add_u32_e32 v50, s5, v68
	v_add_u32_e32 v52, s22, v69
	v_add_u32_e32 v54, s5, v70
	v_add_u32_e32 v56, s22, v71
	v_add_u32_e32 v58, s5, v72
	v_add_u32_e32 v60, s22, v73
	v_ashrrev_i32_e32 v31, 31, v30
	v_lshlrev_b64 v[32:33], 13, v[32:33]
	v_ashrrev_i32_e32 v37, 31, v36
	v_ashrrev_i32_e32 v35, 31, v34
	v_ashrrev_i32_e32 v41, 31, v40
	v_ashrrev_i32_e32 v39, 31, v38
	v_ashrrev_i32_e32 v45, 31, v44
	v_ashrrev_i32_e32 v43, 31, v42
	v_ashrrev_i32_e32 v49, 31, v48
	v_ashrrev_i32_e32 v47, 31, v46
	v_ashrrev_i32_e32 v53, 31, v52
	v_ashrrev_i32_e32 v51, 31, v50
	v_ashrrev_i32_e32 v57, 31, v56
	v_ashrrev_i32_e32 v55, 31, v54
	v_ashrrev_i32_e32 v61, 31, v60
	v_ashrrev_i32_e32 v59, 31, v58
	v_lshlrev_b64 v[30:31], 13, v[30:31]
	v_lshl_add_u64 v[32:33], v[28:29], 0, v[32:33]
	v_lshlrev_b64 v[34:35], 13, v[34:35]
	v_lshlrev_b64 v[36:37], 13, v[36:37]
	v_lshlrev_b64 v[38:39], 13, v[38:39]
	v_lshlrev_b64 v[40:41], 13, v[40:41]
	v_lshlrev_b64 v[42:43], 13, v[42:43]
	v_lshlrev_b64 v[44:45], 13, v[44:45]
	v_lshlrev_b64 v[46:47], 13, v[46:47]
	v_lshlrev_b64 v[48:49], 13, v[48:49]
	v_lshlrev_b64 v[50:51], 13, v[50:51]
	v_lshlrev_b64 v[52:53], 13, v[52:53]
	v_lshlrev_b64 v[54:55], 13, v[54:55]
	v_lshlrev_b64 v[56:57], 13, v[56:57]
	v_lshlrev_b64 v[58:59], 13, v[58:59]
	v_lshlrev_b64 v[60:61], 13, v[60:61]
	v_lshl_add_u64 v[30:31], v[28:29], 0, v[30:31]
	v_lshl_add_u64 v[36:37], v[28:29], 0, v[36:37]
	v_lshl_add_u64 v[34:35], v[28:29], 0, v[34:35]
	v_lshl_add_u64 v[40:41], v[28:29], 0, v[40:41]
	v_lshl_add_u64 v[38:39], v[28:29], 0, v[38:39]
	v_lshl_add_u64 v[44:45], v[28:29], 0, v[44:45]
	v_lshl_add_u64 v[42:43], v[28:29], 0, v[42:43]
	v_lshl_add_u64 v[48:49], v[28:29], 0, v[48:49]
	v_lshl_add_u64 v[46:47], v[28:29], 0, v[46:47]
	v_lshl_add_u64 v[52:53], v[28:29], 0, v[52:53]
	v_lshl_add_u64 v[50:51], v[28:29], 0, v[50:51]
	v_lshl_add_u64 v[56:57], v[28:29], 0, v[56:57]
	v_lshl_add_u64 v[54:55], v[28:29], 0, v[54:55]
	v_lshl_add_u64 v[60:61], v[28:29], 0, v[60:61]
	v_lshl_add_u64 v[58:59], v[28:29], 0, v[58:59]
	global_load_dword v74, v[32:33], off nt
	global_load_dword v75, v[30:31], off nt
	global_load_dword v76, v[36:37], off nt
	global_load_dword v77, v[34:35], off nt
	global_load_dword v78, v[40:41], off nt
	global_load_dword v79, v[38:39], off nt
	global_load_dword v80, v[44:45], off nt
	global_load_dword v81, v[42:43], off nt
	global_load_dword v82, v[48:49], off nt
	global_load_dword v83, v[46:47], off nt
	global_load_dword v84, v[52:53], off nt
	global_load_dword v85, v[50:51], off nt
	global_load_dword v86, v[56:57], off nt
	global_load_dword v87, v[54:55], off nt
	global_load_dword v88, v[60:61], off nt
	global_load_dword v89, v[58:59], off nt
	s_add_i32 s25, s25, 16
	s_add_i32 s23, s23, 16
	s_add_i32 s39, s39, -16
	v_mad_u64_u32 v[30:31], s[40:41], v7, s35, v[6:7]
	s_cmp_lg_u32 s39, 0
	v_mad_u64_u32 v[32:33], s[40:41], v4, s35, v[6:7]
	v_mad_u64_u32 v[34:35], s[40:41], v27, s35, v[6:7]
	v_mad_u64_u32 v[36:37], s[40:41], v25, s35, v[6:7]
	v_mad_u64_u32 v[38:39], s[40:41], v63, s35, v[6:7]
	v_mad_u64_u32 v[40:41], s[40:41], v62, s35, v[6:7]
	v_mad_u64_u32 v[42:43], s[40:41], v65, s35, v[6:7]
	v_mad_u64_u32 v[44:45], s[40:41], v64, s35, v[6:7]
	v_mad_u64_u32 v[46:47], s[40:41], v67, s35, v[6:7]
	v_mad_u64_u32 v[48:49], s[40:41], v66, s35, v[6:7]
	v_mad_u64_u32 v[50:51], s[40:41], v69, s35, v[6:7]
	v_mad_u64_u32 v[52:53], s[40:41], v68, s35, v[6:7]
	v_mad_u64_u32 v[54:55], s[40:41], v71, s35, v[6:7]
	v_mad_u64_u32 v[56:57], s[40:41], v70, s35, v[6:7]
	v_mad_u64_u32 v[58:59], s[40:41], v73, s35, v[6:7]
	v_mad_u64_u32 v[60:61], s[40:41], v72, s35, v[6:7]
	s_waitcnt vmcnt(15)
	ds_write_b32 v30, v74 offset:61440
	s_waitcnt vmcnt(14)
	ds_write_b32 v32, v75 offset:61440
	s_waitcnt vmcnt(13)
	ds_write_b32 v34, v76 offset:61440
	s_waitcnt vmcnt(12)
	ds_write_b32 v36, v77 offset:61440
	s_waitcnt vmcnt(11)
	ds_write_b32 v38, v78 offset:61440
	s_waitcnt vmcnt(10)
	ds_write_b32 v40, v79 offset:61440
	s_waitcnt vmcnt(9)
	ds_write_b32 v42, v80 offset:61440
	s_waitcnt vmcnt(8)
	ds_write_b32 v44, v81 offset:61440
	s_waitcnt vmcnt(7)
	ds_write_b32 v46, v82 offset:61440
	s_waitcnt vmcnt(6)
	ds_write_b32 v48, v83 offset:61440
	s_waitcnt vmcnt(5)
	ds_write_b32 v50, v84 offset:61440
	s_waitcnt vmcnt(4)
	ds_write_b32 v52, v85 offset:61440
	s_waitcnt vmcnt(3)
	ds_write_b32 v54, v86 offset:61440
	s_waitcnt vmcnt(2)
	ds_write_b32 v56, v87 offset:61440
	s_waitcnt vmcnt(1)
	ds_write_b32 v58, v88 offset:61440
	s_waitcnt vmcnt(0)
	ds_write_b32 v60, v89 offset:61440
	s_cbranch_scc1 .LBB0_78
; #define LAS __attribute__((address_space(3)))
; __device__ __forceinline__ unsigned cvtpk(float lo, float hi) { f32x2 v = {lo, hi}; bf16x2_t b = __builtin_convertvector(v, bf16x2_t); return __builtin_bit_cast(unsigned, b); }
; #define LDS_WAIT() asm volatile("s_waitcnt lgkmcnt(0)" ::: "memory")
; __device__ __forceinline__ void transpose_item(const float* W, int ldw, int k0, int n0, bf16_t* dstrow0, int ldt, LAS float* scr, int lane) {
;     ...
;     const int c = lane & 7;
; #pragma unroll
;     for (int j = 0; j < 4; ++j) { const int n = (lane >> 3) + 8 * j; const LAS float* s = scr + (8 * c) * 33 + n;
;         u32x4 o; o.x = cvtpk(s[0 * 33], s[1 * 33]); o.y = cvtpk(s[2 * 33], s[3 * 33]); o.z = cvtpk(s[4 * 33], s[5 * 33]); o.w = cvtpk(s[6 * 33], s[7 * 33]);
;         *(u32x4*)(dstrow0 + (size_t)n * ldt + k0 + 8 * c) = o; }
;     LDS_WAIT(); asm volatile("" ::: "memory");
	s_lshl_b64 s[18:19], s[18:19], 9
	s_add_u32 s5, s16, s20
	s_waitcnt lgkmcnt(0)
	s_addc_u32 s20, s17, s21
	s_add_u32 s5, s5, s18
	s_mov_b32 s23, s3
	ds_read2_b32 v[32:33], v3 offset0:33 offset1:41
	ds_read2_b32 v[34:35], v3 offset1:8
	ds_read2_b32 v[36:37], v3 offset0:66 offset1:74
	ds_read2_b32 v[38:39], v3 offset0:99 offset1:107
	ds_read2_b32 v[40:41], v3 offset0:132 offset1:140
	ds_read2_b32 v[42:43], v3 offset0:165 offset1:173
	ds_read2_b32 v[44:45], v3 offset0:198 offset1:206
	ds_read2_b32 v[46:47], v3 offset0:231 offset1:239
	s_addc_u32 s20, s20, s19
	s_lshl_b64 s[18:19], s[22:23], 1
	s_add_u32 s18, s5, s18
	s_addc_u32 s19, s20, s19
	v_mov_b32_e32 v27, v5
	v_lshl_add_u64 v[48:49], s[18:19], 0, v[26:27]
	s_waitcnt lgkmcnt(6)
	v_cvt_pk_bf16_f32 v28, v34, v32
	s_waitcnt lgkmcnt(4)
	v_cvt_pk_bf16_f32 v29, v36, v38
	s_waitcnt lgkmcnt(2)
	v_cvt_pk_bf16_f32 v30, v40, v42
	s_waitcnt lgkmcnt(0)
	v_cvt_pk_bf16_f32 v31, v44, v46
	v_lshl_add_u64 v[50:51], v[48:49], 0, v[16:17]
	global_store_dwordx4 v[50:51], v[28:31], off
	s_mov_b64 s[18:19], 0
	s_nop 0
	v_cvt_pk_bf16_f32 v28, v35, v33
	v_cvt_pk_bf16_f32 v29, v37, v39
	v_cvt_pk_bf16_f32 v30, v41, v43
	v_cvt_pk_bf16_f32 v31, v45, v47
	ds_read2_b32 v[34:35], v3 offset0:49 offset1:57
	ds_read2_b32 v[36:37], v3 offset0:16 offset1:24
	ds_read2_b32 v[38:39], v3 offset0:82 offset1:90
	ds_read2_b32 v[40:41], v3 offset0:115 offset1:123
	ds_read2_b32 v[42:43], v3 offset0:148 offset1:156
	ds_read2_b32 v[44:45], v3 offset0:181 offset1:189
	ds_read2_b32 v[46:47], v3 offset0:214 offset1:222
	ds_read2_b32 v[50:51], v3 offset0:247 offset1:255
	v_lshl_add_u64 v[32:33], v[48:49], 0, v[18:19]
	global_store_dwordx4 v[32:33], v[28:31], off
	v_lshl_add_u64 v[32:33], v[48:49], 0, v[20:21]
	s_waitcnt lgkmcnt(6)
	v_cvt_pk_bf16_f32 v28, v36, v34
	s_waitcnt lgkmcnt(4)
	v_cvt_pk_bf16_f32 v29, v38, v40
	s_waitcnt lgkmcnt(2)
	v_cvt_pk_bf16_f32 v30, v42, v44
	s_waitcnt lgkmcnt(0)
	v_cvt_pk_bf16_f32 v31, v46, v50
	global_store_dwordx4 v[32:33], v[28:31], off
	v_lshl_add_u64 v[32:33], v[48:49], 0, v[22:23]
	s_nop 0
	v_cvt_pk_bf16_f32 v28, v37, v35
	v_cvt_pk_bf16_f32 v29, v39, v41
	v_cvt_pk_bf16_f32 v30, v43, v45
	v_cvt_pk_bf16_f32 v31, v47, v51
	global_store_dwordx4 v[32:33], v[28:31], off
	s_waitcnt lgkmcnt(0)

; #define LAS __attribute__((address_space(3)))
; __device__ __forceinline__ unsigned cvtpk(float lo, float hi) { f32x2 v = {lo, hi}; bf16x2_t b = __builtin_convertvector(v, bf16x2_t); return __builtin_bit_cast(unsigned, b); }
; #define LDS_WAIT() asm volatile("s_waitcnt lgkmcnt(0)" ::: "memory")
; __device__ __forceinline__ void transpose_item(const float* W, int ldw, int k0, int n0, bf16_t* dstrow0, int ldt, LAS float* scr, int lane) {
;     ...
;     for (int i = 0; i < 32; ++i) { const int kk = 2 * i + (lane >> 5); scr[kk * 33 + (lane & 31)] = W[(size_t)(k0 + kk) * ldw + n0 + (lane & 31)]; }
;     LDS_WAIT(); asm volatile("" ::: "memory");
;     const int c = lane & 7;
; #pragma unroll
;     for (int j = 0; j < 4; ++j) { const int n = (lane >> 3) + 8 * j; const LAS float* s = scr + (8 * c) * 33 + n;
;         u32x4 o; o.x = cvtpk(s[0 * 33], s[1 * 33]); o.y = cvtpk(s[2 * 33], s[3 * 33]); o.z = cvtpk(s[4 * 33], s[5 * 33]); o.w = cvtpk(s[6 * 33], s[7 * 33]);
;         *(u32x4*)(dstrow0 + (size_t)n * ldt + k0 + 8 * c) = o; }
;     LDS_WAIT(); asm volatile("" ::: "memory");
.LBB0_82:
	s_lshl_b32 s25, s21, 1
	s_lshl_b32 s39, s22, 1
	v_or_b32_e32 v4, s25, v1
	v_or_b32_e32 v7, s39, v2
	s_add_i32 s40, s25, 4
	s_add_i32 s41, s39, 4
	s_add_i32 s42, s25, 8
	s_add_i32 s43, s39, 8
	s_add_i32 s44, s25, 12
	s_add_i32 s45, s39, 12
	s_add_i32 s46, s25, 16
	s_add_i32 s47, s39, 16
	s_add_i32 s48, s25, 20
	s_add_i32 s49, s39, 20
	s_add_i32 s50, s25, 24
	s_add_i32 s51, s39, 24
	s_add_i32 s25, s25, 28
	s_add_i32 s39, s39, 28
	v_add_u32_e32 v25, s20, v4
	v_add_u32_e32 v27, s5, v7
	v_or_b32_e32 v62, s40, v1
	v_or_b32_e32 v63, s41, v2
	v_or_b32_e32 v64, s42, v1
	v_or_b32_e32 v65, s43, v2
	v_or_b32_e32 v66, s44, v1
	v_or_b32_e32 v67, s45, v2
	v_or_b32_e32 v68, s46, v1
	v_or_b32_e32 v69, s47, v2
	v_or_b32_e32 v70, s48, v1
	v_or_b32_e32 v71, s49, v2
	v_or_b32_e32 v72, s50, v1
	v_or_b32_e32 v73, s51, v2
	v_or_b32_e32 v74, s25, v1
	v_or_b32_e32 v75, s39, v2
	v_mad_u64_u32 v[30:31], s[40:41], v27, s36, v[28:29]
	v_mad_u64_u32 v[32:33], s[40:41], v25, s36, v[28:29]
	v_add_u32_e32 v25, s20, v62
	v_add_u32_e32 v27, s5, v63
	v_add_u32_e32 v40, s20, v64
	v_add_u32_e32 v38, s5, v65
	v_add_u32_e32 v44, s20, v66
	v_add_u32_e32 v42, s5, v67
	v_add_u32_e32 v48, s20, v68
	v_add_u32_e32 v46, s5, v69
	v_add_u32_e32 v52, s20, v70
	v_add_u32_e32 v50, s5, v71
	v_add_u32_e32 v56, s20, v72
	v_add_u32_e32 v54, s5, v73
	v_add_u32_e32 v60, s20, v74
	v_add_u32_e32 v58, s5, v75
	v_mad_u64_u32 v[34:35], s[40:41], v27, s36, v[28:29]
	v_mad_u64_u32 v[36:37], s[40:41], v25, s36, v[28:29]
	v_mad_u64_u32 v[38:39], s[40:41], v38, s36, v[28:29]
	v_mad_u64_u32 v[40:41], s[40:41], v40, s36, v[28:29]
	v_mad_u64_u32 v[42:43], s[40:41], v42, s36, v[28:29]
	v_mad_u64_u32 v[44:45], s[40:41], v44, s36, v[28:29]
	v_mad_u64_u32 v[46:47], s[40:41], v46, s36, v[28:29]
	v_mad_u64_u32 v[48:49], s[40:41], v48, s36, v[28:29]
	v_mad_u64_u32 v[50:51], s[40:41], v50, s36, v[28:29]
	v_mad_u64_u32 v[52:53], s[40:41], v52, s36, v[28:29]
	v_mad_u64_u32 v[54:55], s[40:41], v54, s36, v[28:29]
	v_mad_u64_u32 v[56:57], s[40:41], v56, s36, v[28:29]
	v_mad_u64_u32 v[58:59], s[40:41], v58, s36, v[28:29]
	v_mad_u64_u32 v[60:61], s[40:41], v60, s36, v[28:29]
	global_load_dword v25, v[30:31], off nt
	global_load_dword v27, v[32:33], off nt
	global_load_dword v76, v[34:35], off nt
	global_load_dword v77, v[36:37], off nt
	global_load_dword v78, v[38:39], off nt
	global_load_dword v79, v[40:41], off nt
	global_load_dword v80, v[42:43], off nt
	global_load_dword v81, v[44:45], off nt
	global_load_dword v82, v[46:47], off nt
	global_load_dword v83, v[48:49], off nt
	global_load_dword v84, v[50:51], off nt
	global_load_dword v85, v[52:53], off nt
	global_load_dword v86, v[54:55], off nt
	global_load_dword v87, v[56:57], off nt
	global_load_dword v88, v[58:59], off nt
	global_load_dword v89, v[60:61], off nt
	s_add_i32 s22, s22, 16
	s_add_i32 s21, s21, 16
	s_add_i32 s23, s23, -16
	v_mad_u64_u32 v[30:31], s[40:41], v7, s35, v[6:7]
	s_cmp_lg_u32 s23, 0
	v_mad_u64_u32 v[32:33], s[40:41], v4, s35, v[6:7]
	v_mad_u64_u32 v[34:35], s[40:41], v63, s35, v[6:7]
	v_mad_u64_u32 v[36:37], s[40:41], v62, s35, v[6:7]
	v_mad_u64_u32 v[38:39], s[40:41], v65, s35, v[6:7]
	v_mad_u64_u32 v[40:41], s[40:41], v64, s35, v[6:7]
	v_mad_u64_u32 v[42:43], s[40:41], v67, s35, v[6:7]
	v_mad_u64_u32 v[44:45], s[40:41], v66, s35, v[6:7]
	v_mad_u64_u32 v[46:47], s[40:41], v69, s35, v[6:7]
	v_mad_u64_u32 v[48:49], s[40:41], v68, s35, v[6:7]
	v_mad_u64_u32 v[50:51], s[40:41], v71, s35, v[6:7]
	v_mad_u64_u32 v[52:53], s[40:41], v70, s35, v[6:7]
	v_mad_u64_u32 v[54:55], s[40:41], v73, s35, v[6:7]
	v_mad_u64_u32 v[56:57], s[40:41], v72, s35, v[6:7]
	v_mad_u64_u32 v[58:59], s[40:41], v75, s35, v[6:7]
	v_mad_u64_u32 v[60:61], s[40:41], v74, s35, v[6:7]
	s_waitcnt vmcnt(15)
	ds_write_b32 v30, v25 offset:61440
	s_waitcnt vmcnt(14)
	ds_write_b32 v32, v27 offset:61440
	s_waitcnt vmcnt(13)
	ds_write_b32 v34, v76 offset:61440
	s_waitcnt vmcnt(12)
	ds_write_b32 v36, v77 offset:61440
	s_waitcnt vmcnt(11)
	ds_write_b32 v38, v78 offset:61440
	s_waitcnt vmcnt(10)
	ds_write_b32 v40, v79 offset:61440
	s_waitcnt vmcnt(9)
	ds_write_b32 v42, v80 offset:61440
	s_waitcnt vmcnt(8)
	ds_write_b32 v44, v81 offset:61440
	s_waitcnt vmcnt(7)
	ds_write_b32 v46, v82 offset:61440
	s_waitcnt vmcnt(6)
	ds_write_b32 v48, v83 offset:61440
	s_waitcnt vmcnt(5)
	ds_write_b32 v50, v84 offset:61440
	s_waitcnt vmcnt(4)
	ds_write_b32 v52, v85 offset:61440
	s_waitcnt vmcnt(3)
	ds_write_b32 v54, v86 offset:61440
	s_waitcnt vmcnt(2)
	ds_write_b32 v56, v87 offset:61440
	s_waitcnt vmcnt(1)
	ds_write_b32 v58, v88 offset:61440
	s_waitcnt vmcnt(0)
	ds_write_b32 v60, v89 offset:61440
	s_cbranch_scc1 .LBB0_82
	s_mul_i32 s21, s4, 0x600
	s_mul_hi_i32 s20, s4, 0x600
	s_add_u32 s18, s21, s18
	s_addc_u32 s19, s20, s19
	s_waitcnt lgkmcnt(0)
	s_lshl_b64 s[18:19], s[18:19], 9
	s_add_u32 s18, s30, s18
	ds_read2_b32 v[32:33], v3 offset0:33 offset1:41
	ds_read2_b32 v[34:35], v3 offset1:8
	ds_read2_b32 v[36:37], v3 offset0:66 offset1:74
	ds_read2_b32 v[38:39], v3 offset0:99 offset1:107
	ds_read2_b32 v[40:41], v3 offset0:132 offset1:140
	ds_read2_b32 v[42:43], v3 offset0:165 offset1:173
	ds_read2_b32 v[44:45], v3 offset0:198 offset1:206
	ds_read2_b32 v[46:47], v3 offset0:231 offset1:239
	s_addc_u32 s19, s31, s19
	s_lshl_b32 s5, s5, 1
	s_add_u32 s18, s18, s5
	s_addc_u32 s19, s19, 0
	v_mov_b32_e32 v27, v5
	v_lshl_add_u64 v[48:49], s[18:19], 0, v[26:27]
	s_waitcnt lgkmcnt(6)
	v_cvt_pk_bf16_f32 v28, v34, v32
	s_waitcnt lgkmcnt(4)
	v_cvt_pk_bf16_f32 v29, v36, v38
	s_waitcnt lgkmcnt(2)
	v_cvt_pk_bf16_f32 v30, v40, v42
	s_waitcnt lgkmcnt(0)
	v_cvt_pk_bf16_f32 v31, v44, v46
	v_lshl_add_u64 v[50:51], v[48:49], 0, v[16:17]
	global_store_dwordx4 v[50:51], v[28:31], off
	s_nop 1
	v_cvt_pk_bf16_f32 v28, v35, v33
	v_cvt_pk_bf16_f32 v29, v37, v39
	v_cvt_pk_bf16_f32 v30, v41, v43
	v_cvt_pk_bf16_f32 v31, v45, v47
	ds_read2_b32 v[34:35], v3 offset0:49 offset1:57
	ds_read2_b32 v[36:37], v3 offset0:16 offset1:24
	ds_read2_b32 v[38:39], v3 offset0:82 offset1:90
	ds_read2_b32 v[40:41], v3 offset0:115 offset1:123
	ds_read2_b32 v[42:43], v3 offset0:148 offset1:156
	ds_read2_b32 v[44:45], v3 offset0:181 offset1:189
	ds_read2_b32 v[46:47], v3 offset0:214 offset1:222
	ds_read2_b32 v[50:51], v3 offset0:247 offset1:255
	v_lshl_add_u64 v[32:33], v[48:49], 0, v[18:19]
	global_store_dwordx4 v[32:33], v[28:31], off
	v_lshl_add_u64 v[32:33], v[48:49], 0, v[20:21]
	s_waitcnt lgkmcnt(6)
	v_cvt_pk_bf16_f32 v28, v36, v34
	s_waitcnt lgkmcnt(4)
	v_cvt_pk_bf16_f32 v29, v38, v40
	s_waitcnt lgkmcnt(2)
	v_cvt_pk_bf16_f32 v30, v42, v44
	s_waitcnt lgkmcnt(0)
	v_cvt_pk_bf16_f32 v31, v46, v50
	global_store_dwordx4 v[32:33], v[28:31], off
	v_lshl_add_u64 v[32:33], v[48:49], 0, v[22:23]
	s_nop 0
	v_cvt_pk_bf16_f32 v28, v37, v35
	v_cvt_pk_bf16_f32 v29, v39, v41
	v_cvt_pk_bf16_f32 v30, v43, v45
	v_cvt_pk_bf16_f32 v31, v47, v51
	global_store_dwordx4 v[32:33], v[28:31], off
	s_waitcnt lgkmcnt(0)

; #define LAS __attribute__((address_space(3)))
; __device__ __forceinline__ unsigned cvtpk(float lo, float hi) { f32x2 v = {lo, hi}; bf16x2_t b = __builtin_convertvector(v, bf16x2_t); return __builtin_bit_cast(unsigned, b); }
; #define LDS_WAIT() asm volatile("s_waitcnt lgkmcnt(0)" ::: "memory")
; __device__ __forceinline__ void transpose_item(const float* W, int ldw, int k0, int n0, bf16_t* dstrow0, int ldt, LAS float* scr, int lane) {
;     ...
;     for (int i = 0; i < 32; ++i) { const int kk = 2 * i + (lane >> 5); scr[kk * 33 + (lane & 31)] = W[(size_t)(k0 + kk) * ldw + n0 + (lane & 31)]; }
;     LDS_WAIT(); asm volatile("" ::: "memory");
;     const int c = lane & 7;
; #pragma unroll
;     for (int j = 0; j < 4; ++j) { const int n = (lane >> 3) + 8 * j; const LAS float* s = scr + (8 * c) * 33 + n;
;         u32x4 o; o.x = cvtpk(s[0 * 33], s[1 * 33]); o.y = cvtpk(s[2 * 33], s[3 * 33]); o.z = cvtpk(s[4 * 33], s[5 * 33]); o.w = cvtpk(s[6 * 33], s[7 * 33]);
;         *(u32x4*)(dstrow0 + (size_t)n * ldt + k0 + 8 * c) = o; }
;     LDS_WAIT(); asm volatile("" ::: "memory");
.LBB0_87:
	s_lshl_b32 s39, s22, 1
	s_lshl_b32 s40, s23, 1
	v_or_b32_e32 v4, s39, v1
	v_or_b32_e32 v7, s40, v2
	s_add_i32 s41, s39, 4
	s_add_i32 s42, s40, 4
	s_add_i32 s43, s39, 8
	s_add_i32 s44, s40, 8
	s_add_i32 s45, s39, 12
	s_add_i32 s46, s40, 12
	s_add_i32 s47, s39, 16
	s_add_i32 s48, s40, 16
	s_add_i32 s49, s39, 20
	s_add_i32 s50, s40, 20
	s_add_i32 s51, s39, 24
	s_add_i32 s52, s40, 24
	s_add_i32 s39, s39, 28
	s_add_i32 s40, s40, 28
	v_add_u32_e32 v25, s21, v4
	v_add_u32_e32 v27, s20, v7
	v_or_b32_e32 v62, s41, v1
	v_or_b32_e32 v63, s42, v2
	v_or_b32_e32 v64, s43, v1
	v_or_b32_e32 v65, s44, v2
	v_or_b32_e32 v66, s45, v1
	v_or_b32_e32 v67, s46, v2
	v_or_b32_e32 v68, s47, v1
	v_or_b32_e32 v69, s48, v2
	v_or_b32_e32 v70, s49, v1
	v_or_b32_e32 v71, s50, v2
	v_or_b32_e32 v72, s51, v1
	v_or_b32_e32 v73, s52, v2
	v_or_b32_e32 v74, s39, v1
	v_or_b32_e32 v75, s40, v2
	v_mad_u64_u32 v[30:31], s[40:41], v27, s37, v[28:29]
	v_mad_u64_u32 v[32:33], s[40:41], v25, s37, v[28:29]
	v_add_u32_e32 v25, s21, v62
	v_add_u32_e32 v27, s20, v63
	v_add_u32_e32 v40, s21, v64
	v_add_u32_e32 v38, s20, v65
	v_add_u32_e32 v44, s21, v66
	v_add_u32_e32 v42, s20, v67
	v_add_u32_e32 v48, s21, v68
	v_add_u32_e32 v46, s20, v69
	v_add_u32_e32 v52, s21, v70
	v_add_u32_e32 v50, s20, v71
	v_add_u32_e32 v56, s21, v72
	v_add_u32_e32 v54, s20, v73
	v_add_u32_e32 v60, s21, v74
	v_add_u32_e32 v58, s20, v75
	v_mad_u64_u32 v[34:35], s[40:41], v27, s37, v[28:29]
	v_mad_u64_u32 v[36:37], s[40:41], v25, s37, v[28:29]
	v_mad_u64_u32 v[38:39], s[40:41], v38, s37, v[28:29]
	v_mad_u64_u32 v[40:41], s[40:41], v40, s37, v[28:29]
	v_mad_u64_u32 v[42:43], s[40:41], v42, s37, v[28:29]
	v_mad_u64_u32 v[44:45], s[40:41], v44, s37, v[28:29]
	v_mad_u64_u32 v[46:47], s[40:41], v46, s37, v[28:29]
	v_mad_u64_u32 v[48:49], s[40:41], v48, s37, v[28:29]
	v_mad_u64_u32 v[50:51], s[40:41], v50, s37, v[28:29]
	v_mad_u64_u32 v[52:53], s[40:41], v52, s37, v[28:29]
	v_mad_u64_u32 v[54:55], s[40:41], v54, s37, v[28:29]
	v_mad_u64_u32 v[56:57], s[40:41], v56, s37, v[28:29]
	v_mad_u64_u32 v[58:59], s[40:41], v58, s37, v[28:29]
	v_mad_u64_u32 v[60:61], s[40:41], v60, s37, v[28:29]
	global_load_dword v25, v[30:31], off nt
	global_load_dword v27, v[32:33], off nt
	global_load_dword v76, v[34:35], off nt
	global_load_dword v77, v[36:37], off nt
	global_load_dword v78, v[38:39], off nt
	global_load_dword v79, v[40:41], off nt
	global_load_dword v80, v[42:43], off nt
	global_load_dword v81, v[44:45], off nt
	global_load_dword v82, v[46:47], off nt
	global_load_dword v83, v[48:49], off nt
	global_load_dword v84, v[50:51], off nt
	global_load_dword v85, v[52:53], off nt
	global_load_dword v86, v[54:55], off nt
	global_load_dword v87, v[56:57], off nt
	global_load_dword v88, v[58:59], off nt
	global_load_dword v89, v[60:61], off nt
	s_add_i32 s23, s23, 16
	s_add_i32 s22, s22, 16
	s_add_i32 s25, s25, -16
	v_mad_u64_u32 v[30:31], s[40:41], v7, s35, v[6:7]
	s_cmp_lg_u32 s25, 0
	v_mad_u64_u32 v[32:33], s[40:41], v4, s35, v[6:7]
	v_mad_u64_u32 v[34:35], s[40:41], v63, s35, v[6:7]
	v_mad_u64_u32 v[36:37], s[40:41], v62, s35, v[6:7]
	v_mad_u64_u32 v[38:39], s[40:41], v65, s35, v[6:7]
	v_mad_u64_u32 v[40:41], s[40:41], v64, s35, v[6:7]
	v_mad_u64_u32 v[42:43], s[40:41], v67, s35, v[6:7]
	v_mad_u64_u32 v[44:45], s[40:41], v66, s35, v[6:7]
	v_mad_u64_u32 v[46:47], s[40:41], v69, s35, v[6:7]
	v_mad_u64_u32 v[48:49], s[40:41], v68, s35, v[6:7]
	v_mad_u64_u32 v[50:51], s[40:41], v71, s35, v[6:7]
	v_mad_u64_u32 v[52:53], s[40:41], v70, s35, v[6:7]
	v_mad_u64_u32 v[54:55], s[40:41], v73, s35, v[6:7]
	v_mad_u64_u32 v[56:57], s[40:41], v72, s35, v[6:7]
	v_mad_u64_u32 v[58:59], s[40:41], v75, s35, v[6:7]
	v_mad_u64_u32 v[60:61], s[40:41], v74, s35, v[6:7]
	s_waitcnt vmcnt(15)
	ds_write_b32 v30, v25 offset:61440
	s_waitcnt vmcnt(14)
	ds_write_b32 v32, v27 offset:61440
	s_waitcnt vmcnt(13)
	ds_write_b32 v34, v76 offset:61440
	s_waitcnt vmcnt(12)
	ds_write_b32 v36, v77 offset:61440
	s_waitcnt vmcnt(11)
	ds_write_b32 v38, v78 offset:61440
	s_waitcnt vmcnt(10)
	ds_write_b32 v40, v79 offset:61440
	s_waitcnt vmcnt(9)
	ds_write_b32 v42, v80 offset:61440
	s_waitcnt vmcnt(8)
	ds_write_b32 v44, v81 offset:61440
	s_waitcnt vmcnt(7)
	ds_write_b32 v46, v82 offset:61440
	s_waitcnt vmcnt(6)
	ds_write_b32 v48, v83 offset:61440
	s_waitcnt vmcnt(5)
	ds_write_b32 v50, v84 offset:61440
	s_waitcnt vmcnt(4)
	ds_write_b32 v52, v85 offset:61440
	s_waitcnt vmcnt(3)
	ds_write_b32 v54, v86 offset:61440
	s_waitcnt vmcnt(2)
	ds_write_b32 v56, v87 offset:61440
	s_waitcnt vmcnt(1)
	ds_write_b32 v58, v88 offset:61440
	s_waitcnt vmcnt(0)
	ds_write_b32 v60, v89 offset:61440
	s_cbranch_scc1 .LBB0_87
	s_lshl_b64 s[22:23], s[4:5], 20
	s_lshl_b64 s[18:19], s[18:19], 11
	s_add_u32 s5, s10, s22
	s_waitcnt lgkmcnt(0)
	s_addc_u32 s21, s11, s23
	s_add_u32 s5, s5, s18
	ds_read2_b32 v[32:33], v3 offset0:33 offset1:41
	ds_read2_b32 v[34:35], v3 offset1:8
	ds_read2_b32 v[36:37], v3 offset0:66 offset1:74
	ds_read2_b32 v[38:39], v3 offset0:99 offset1:107
	ds_read2_b32 v[40:41], v3 offset0:132 offset1:140
	ds_read2_b32 v[42:43], v3 offset0:165 offset1:173
	ds_read2_b32 v[44:45], v3 offset0:198 offset1:206
	ds_read2_b32 v[46:47], v3 offset0:231 offset1:239
	s_addc_u32 s19, s21, s19
	s_lshl_b32 s18, s20, 1
	s_add_u32 s18, s5, s18
	s_addc_u32 s19, s19, 0
	v_mov_b32_e32 v27, v5
	v_lshl_add_u64 v[48:49], s[18:19], 0, v[26:27]
	s_waitcnt lgkmcnt(6)
	v_cvt_pk_bf16_f32 v28, v34, v32
	s_waitcnt lgkmcnt(4)
	v_cvt_pk_bf16_f32 v29, v36, v38
	s_waitcnt lgkmcnt(2)
	v_cvt_pk_bf16_f32 v30, v40, v42
	s_waitcnt lgkmcnt(0)
	v_cvt_pk_bf16_f32 v31, v44, v46
	v_lshl_add_u64 v[50:51], v[48:49], 0, v[8:9]
	global_store_dwordx4 v[50:51], v[28:31], off
	s_nop 1
	v_cvt_pk_bf16_f32 v28, v35, v33
	v_cvt_pk_bf16_f32 v29, v37, v39
	v_cvt_pk_bf16_f32 v30, v41, v43
	v_cvt_pk_bf16_f32 v31, v45, v47
	ds_read2_b32 v[34:35], v3 offset0:49 offset1:57
	ds_read2_b32 v[36:37], v3 offset0:16 offset1:24
	ds_read2_b32 v[38:39], v3 offset0:82 offset1:90
	ds_read2_b32 v[40:41], v3 offset0:115 offset1:123
	ds_read2_b32 v[42:43], v3 offset0:148 offset1:156
	ds_read2_b32 v[44:45], v3 offset0:181 offset1:189
	ds_read2_b32 v[46:47], v3 offset0:214 offset1:222
	ds_read2_b32 v[50:51], v3 offset0:247 offset1:255
	v_lshl_add_u64 v[32:33], v[48:49], 0, v[10:11]
	global_store_dwordx4 v[32:33], v[28:31], off
	v_lshl_add_u64 v[32:33], v[48:49], 0, v[12:13]
	s_waitcnt lgkmcnt(6)
	v_cvt_pk_bf16_f32 v28, v36, v34
	s_waitcnt lgkmcnt(4)
	v_cvt_pk_bf16_f32 v29, v38, v40
	s_waitcnt lgkmcnt(2)
	v_cvt_pk_bf16_f32 v30, v42, v44
	s_waitcnt lgkmcnt(0)
	v_cvt_pk_bf16_f32 v31, v46, v50
	global_store_dwordx4 v[32:33], v[28:31], off
	v_lshl_add_u64 v[32:33], v[48:49], 0, v[14:15]
	s_nop 0
	v_cvt_pk_bf16_f32 v28, v37, v35
	v_cvt_pk_bf16_f32 v29, v39, v41
	v_cvt_pk_bf16_f32 v30, v43, v45
	v_cvt_pk_bf16_f32 v31, v47, v51
	global_store_dwordx4 v[32:33], v[28:31], off
	s_waitcnt lgkmcnt(0)

; #define LAS __attribute__((address_space(3)))
; #define LDS_WAIT() asm volatile("s_waitcnt lgkmcnt(0)" ::: "memory")
; __device__ __forceinline__ void transpose_item(const float* W, int ldw, int k0, int n0, bf16_t* dstrow0, int ldt, LAS float* scr, int lane) {
; #pragma unroll 8
;     for (int i = 0; i < 32; ++i) { const int kk = 2 * i + (lane >> 5); scr[kk * 33 + (lane & 31)] = W[(size_t)(k0 + kk) * ldw + n0 + (lane & 31)]; }
;     LDS_WAIT(); asm volatile("" ::: "memory");
.LBB0_92:
	s_lshl_b32 s25, s19, 1
	s_lshl_b32 s39, s22, 1
	v_or_b32_e32 v4, s25, v1
	v_or_b32_e32 v7, s39, v2
	s_add_i32 s40, s25, 4
	s_add_i32 s41, s39, 4
	s_add_i32 s42, s25, 8
	s_add_i32 s43, s39, 8
	s_add_i32 s44, s25, 12
	s_add_i32 s45, s39, 12
	s_add_i32 s46, s25, 16
	s_add_i32 s47, s39, 16
	s_add_i32 s48, s25, 20
	s_add_i32 s49, s39, 20
	s_add_i32 s50, s25, 24
	s_add_i32 s51, s39, 24
	s_add_i32 s25, s25, 28
	s_add_i32 s39, s39, 28
	v_add_u32_e32 v32, s18, v7
	v_or_b32_e32 v25, s40, v1
	v_or_b32_e32 v27, s41, v2
	v_or_b32_e32 v62, s42, v1
	v_or_b32_e32 v63, s43, v2
	v_or_b32_e32 v64, s44, v1
	v_or_b32_e32 v65, s45, v2
	v_or_b32_e32 v66, s46, v1
	v_or_b32_e32 v67, s47, v2
	v_or_b32_e32 v68, s48, v1
	v_or_b32_e32 v69, s49, v2
	v_or_b32_e32 v70, s50, v1
	v_or_b32_e32 v71, s51, v2
	v_or_b32_e32 v72, s25, v1
	v_or_b32_e32 v73, s39, v2
	v_add_u32_e32 v30, s21, v4
	v_ashrrev_i32_e32 v33, 31, v32
	v_add_u32_e32 v34, s21, v25
	v_add_u32_e32 v36, s18, v27
	v_add_u32_e32 v38, s21, v62
	v_add_u32_e32 v40, s18, v63
	v_add_u32_e32 v42, s21, v64
	v_add_u32_e32 v44, s18, v65
	v_add_u32_e32 v46, s21, v66
	v_add_u32_e32 v48, s18, v67
	v_add_u32_e32 v50, s21, v68
	v_add_u32_e32 v52, s18, v69
	v_add_u32_e32 v54, s21, v70
	v_add_u32_e32 v56, s18, v71
	v_add_u32_e32 v58, s21, v72
	v_add_u32_e32 v60, s18, v73
	v_ashrrev_i32_e32 v31, 31, v30
	v_lshlrev_b64 v[32:33], 12, v[32:33]
	v_ashrrev_i32_e32 v37, 31, v36
	v_ashrrev_i32_e32 v35, 31, v34
	v_ashrrev_i32_e32 v41, 31, v40
	v_ashrrev_i32_e32 v39, 31, v38
	v_ashrrev_i32_e32 v45, 31, v44
	v_ashrrev_i32_e32 v43, 31, v42
	v_ashrrev_i32_e32 v49, 31, v48
	v_ashrrev_i32_e32 v47, 31, v46
	v_ashrrev_i32_e32 v53, 31, v52
	v_ashrrev_i32_e32 v51, 31, v50
	v_ashrrev_i32_e32 v57, 31, v56
	v_ashrrev_i32_e32 v55, 31, v54
	v_ashrrev_i32_e32 v61, 31, v60
	v_ashrrev_i32_e32 v59, 31, v58
	v_lshlrev_b64 v[30:31], 12, v[30:31]
	v_lshl_add_u64 v[32:33], v[28:29], 0, v[32:33]
	v_lshlrev_b64 v[34:35], 12, v[34:35]
	v_lshlrev_b64 v[36:37], 12, v[36:37]
	v_lshlrev_b64 v[38:39], 12, v[38:39]
	v_lshlrev_b64 v[40:41], 12, v[40:41]
	v_lshlrev_b64 v[42:43], 12, v[42:43]
	v_lshlrev_b64 v[44:45], 12, v[44:45]
	v_lshlrev_b64 v[46:47], 12, v[46:47]
	v_lshlrev_b64 v[48:49], 12, v[48:49]
	v_lshlrev_b64 v[50:51], 12, v[50:51]
	v_lshlrev_b64 v[52:53], 12, v[52:53]
	v_lshlrev_b64 v[54:55], 12, v[54:55]
	v_lshlrev_b64 v[56:57], 12, v[56:57]
	v_lshlrev_b64 v[58:59], 12, v[58:59]
	v_lshlrev_b64 v[60:61], 12, v[60:61]
	v_lshl_add_u64 v[30:31], v[28:29], 0, v[30:31]
	v_lshl_add_u64 v[36:37], v[28:29], 0, v[36:37]
	v_lshl_add_u64 v[34:35], v[28:29], 0, v[34:35]
	v_lshl_add_u64 v[40:41], v[28:29], 0, v[40:41]
	v_lshl_add_u64 v[38:39], v[28:29], 0, v[38:39]
	v_lshl_add_u64 v[44:45], v[28:29], 0, v[44:45]
	v_lshl_add_u64 v[42:43], v[28:29], 0, v[42:43]
	v_lshl_add_u64 v[48:49], v[28:29], 0, v[48:49]
	v_lshl_add_u64 v[46:47], v[28:29], 0, v[46:47]
	v_lshl_add_u64 v[52:53], v[28:29], 0, v[52:53]
	v_lshl_add_u64 v[50:51], v[28:29], 0, v[50:51]
	v_lshl_add_u64 v[56:57], v[28:29], 0, v[56:57]
	v_lshl_add_u64 v[54:55], v[28:29], 0, v[54:55]
	v_lshl_add_u64 v[60:61], v[28:29], 0, v[60:61]
	v_lshl_add_u64 v[58:59], v[28:29], 0, v[58:59]
	global_load_dword v74, v[32:33], off nt
	global_load_dword v75, v[30:31], off nt
	global_load_dword v76, v[36:37], off nt
	global_load_dword v77, v[34:35], off nt
	global_load_dword v78, v[40:41], off nt
	global_load_dword v79, v[38:39], off nt
	global_load_dword v80, v[44:45], off nt
	global_load_dword v81, v[42:43], off nt
	global_load_dword v82, v[48:49], off nt
	global_load_dword v83, v[46:47], off nt
	global_load_dword v84, v[52:53], off nt
	global_load_dword v85, v[50:51], off nt
	global_load_dword v86, v[56:57], off nt
	global_load_dword v87, v[54:55], off nt
	global_load_dword v88, v[60:61], off nt
	global_load_dword v89, v[58:59], off nt
	s_add_i32 s22, s22, 16
	s_add_i32 s19, s19, 16
	s_add_i32 s23, s23, -16
	v_mad_u64_u32 v[30:31], s[40:41], v7, s35, v[6:7]
	s_cmp_lg_u32 s23, 0
	v_mad_u64_u32 v[32:33], s[40:41], v4, s35, v[6:7]
	v_mad_u64_u32 v[34:35], s[40:41], v27, s35, v[6:7]
	v_mad_u64_u32 v[36:37], s[40:41], v25, s35, v[6:7]
	v_mad_u64_u32 v[38:39], s[40:41], v63, s35, v[6:7]
	v_mad_u64_u32 v[40:41], s[40:41], v62, s35, v[6:7]
	v_mad_u64_u32 v[42:43], s[40:41], v65, s35, v[6:7]
	v_mad_u64_u32 v[44:45], s[40:41], v64, s35, v[6:7]
	v_mad_u64_u32 v[46:47], s[40:41], v67, s35, v[6:7]
	v_mad_u64_u32 v[48:49], s[40:41], v66, s35, v[6:7]
	v_mad_u64_u32 v[50:51], s[40:41], v69, s35, v[6:7]
	v_mad_u64_u32 v[52:53], s[40:41], v68, s35, v[6:7]
	v_mad_u64_u32 v[54:55], s[40:41], v71, s35, v[6:7]
	v_mad_u64_u32 v[56:57], s[40:41], v70, s35, v[6:7]
	v_mad_u64_u32 v[58:59], s[40:41], v73, s35, v[6:7]
	v_mad_u64_u32 v[60:61], s[40:41], v72, s35, v[6:7]
	s_waitcnt vmcnt(15)
	ds_write_b32 v30, v74 offset:61440
	s_waitcnt vmcnt(14)
	ds_write_b32 v32, v75 offset:61440
	s_waitcnt vmcnt(13)
	ds_write_b32 v34, v76 offset:61440
	s_waitcnt vmcnt(12)
	ds_write_b32 v36, v77 offset:61440
	s_waitcnt vmcnt(11)
	ds_write_b32 v38, v78 offset:61440
	s_waitcnt vmcnt(10)
	ds_write_b32 v40, v79 offset:61440
	s_waitcnt vmcnt(9)
	ds_write_b32 v42, v80 offset:61440
	s_waitcnt vmcnt(8)
	ds_write_b32 v44, v81 offset:61440
	s_waitcnt vmcnt(7)
	ds_write_b32 v46, v82 offset:61440
	s_waitcnt vmcnt(6)
	ds_write_b32 v48, v83 offset:61440
	s_waitcnt vmcnt(5)
	ds_write_b32 v50, v84 offset:61440
	s_waitcnt vmcnt(4)
	ds_write_b32 v52, v85 offset:61440
	s_waitcnt vmcnt(3)
	ds_write_b32 v54, v86 offset:61440
	s_waitcnt vmcnt(2)
	ds_write_b32 v56, v87 offset:61440
	s_waitcnt vmcnt(1)
	ds_write_b32 v58, v88 offset:61440
	s_waitcnt vmcnt(0)
	ds_write_b32 v60, v89 offset:61440
	s_cbranch_scc1 .LBB0_92
; #define LAS __attribute__((address_space(3)))
; __device__ __forceinline__ unsigned cvtpk(float lo, float hi) { f32x2 v = {lo, hi}; bf16x2_t b = __builtin_convertvector(v, bf16x2_t); return __builtin_bit_cast(unsigned, b); }
; #define LDS_WAIT() asm volatile("s_waitcnt lgkmcnt(0)" ::: "memory")
; __device__ __forceinline__ void transpose_item(const float* W, int ldw, int k0, int n0, bf16_t* dstrow0, int ldt, LAS float* scr, int lane) {
;     ...
;     const int c = lane & 7;
; #pragma unroll
;     for (int j = 0; j < 4; ++j) { const int n = (lane >> 3) + 8 * j; const LAS float* s = scr + (8 * c) * 33 + n;
;         u32x4 o; o.x = cvtpk(s[0 * 33], s[1 * 33]); o.y = cvtpk(s[2 * 33], s[3 * 33]); o.z = cvtpk(s[4 * 33], s[5 * 33]); o.w = cvtpk(s[6 * 33], s[7 * 33]);
;         *(u32x4*)(dstrow0 + (size_t)n * ldt + k0 + 8 * c) = o; }
;     LDS_WAIT(); asm volatile("" ::: "memory");
; }
	s_lshl_b64 s[22:23], s[4:5], 21
	s_add_u32 s5, s33, s22
	s_addc_u32 s19, s34, s23
	s_lshl_b32 s20, s20, 11
	s_waitcnt lgkmcnt(0)
	s_add_u32 s5, s5, s20
	s_addc_u32 s20, s19, 0
	s_mov_b32 s19, s3
	ds_read2_b32 v[32:33], v3 offset0:33 offset1:41
	ds_read2_b32 v[34:35], v3 offset1:8
	ds_read2_b32 v[36:37], v3 offset0:66 offset1:74
	ds_read2_b32 v[38:39], v3 offset0:99 offset1:107
	ds_read2_b32 v[40:41], v3 offset0:132 offset1:140
	ds_read2_b32 v[42:43], v3 offset0:165 offset1:173
	ds_read2_b32 v[44:45], v3 offset0:198 offset1:206
	ds_read2_b32 v[46:47], v3 offset0:231 offset1:239
	s_lshl_b64 s[18:19], s[18:19], 1
	s_add_u32 s18, s5, s18
	s_addc_u32 s19, s20, s19
	v_mov_b32_e32 v27, v5
	v_lshl_add_u64 v[48:49], s[18:19], 0, v[26:27]
	s_waitcnt lgkmcnt(6)
	v_cvt_pk_bf16_f32 v28, v34, v32
	s_waitcnt lgkmcnt(4)
	v_cvt_pk_bf16_f32 v29, v36, v38
	s_waitcnt lgkmcnt(2)
	v_cvt_pk_bf16_f32 v30, v40, v42
	s_waitcnt lgkmcnt(0)
	v_cvt_pk_bf16_f32 v31, v44, v46
	v_lshl_add_u64 v[50:51], v[48:49], 0, v[8:9]
	global_store_dwordx4 v[50:51], v[28:31], off
	s_nop 1
	v_cvt_pk_bf16_f32 v28, v35, v33
	v_cvt_pk_bf16_f32 v29, v37, v39
	v_cvt_pk_bf16_f32 v30, v41, v43
	v_cvt_pk_bf16_f32 v31, v45, v47
	ds_read2_b32 v[34:35], v3 offset0:49 offset1:57
	ds_read2_b32 v[36:37], v3 offset0:16 offset1:24
	ds_read2_b32 v[38:39], v3 offset0:82 offset1:90
	ds_read2_b32 v[40:41], v3 offset0:115 offset1:123
	ds_read2_b32 v[42:43], v3 offset0:148 offset1:156
	ds_read2_b32 v[44:45], v3 offset0:181 offset1:189
	ds_read2_b32 v[46:47], v3 offset0:214 offset1:222
	ds_read2_b32 v[50:51], v3 offset0:247 offset1:255
	v_lshl_add_u64 v[32:33], v[48:49], 0, v[10:11]
	global_store_dwordx4 v[32:33], v[28:31], off
	v_lshl_add_u64 v[32:33], v[48:49], 0, v[12:13]
	s_waitcnt lgkmcnt(6)
	v_cvt_pk_bf16_f32 v28, v36, v34
	s_waitcnt lgkmcnt(4)
	v_cvt_pk_bf16_f32 v29, v38, v40
	s_waitcnt lgkmcnt(2)
	v_cvt_pk_bf16_f32 v30, v42, v44
	s_waitcnt lgkmcnt(0)
	v_cvt_pk_bf16_f32 v31, v46, v50
	global_store_dwordx4 v[32:33], v[28:31], off
	v_lshl_add_u64 v[32:33], v[48:49], 0, v[14:15]
	s_nop 0
	v_cvt_pk_bf16_f32 v28, v37, v35
	v_cvt_pk_bf16_f32 v29, v39, v41
	v_cvt_pk_bf16_f32 v30, v43, v45
	v_cvt_pk_bf16_f32 v31, v47, v51
	global_store_dwordx4 v[32:33], v[28:31], off
	s_waitcnt lgkmcnt(0)

; #define LAS __attribute__((address_space(3)))
; __device__ __forceinline__ unsigned cvtpk(float lo, float hi) { f32x2 v = {lo, hi}; bf16x2_t b = __builtin_convertvector(v, bf16x2_t); return __builtin_bit_cast(unsigned, b); }
; #define LDS_WAIT() asm volatile("s_waitcnt lgkmcnt(0)" ::: "memory")
; __device__ __forceinline__ void transpose_item(const float* W, int ldw, int k0, int n0, bf16_t* dstrow0, int ldt, LAS float* scr, int lane) {
; #pragma unroll 8
;     for (int i = 0; i < 32; ++i) { const int kk = 2 * i + (lane >> 5); scr[kk * 33 + (lane & 31)] = W[(size_t)(k0 + kk) * ldw + n0 + (lane & 31)]; }
;     LDS_WAIT(); asm volatile("" ::: "memory");
;     const int c = lane & 7;
; #pragma unroll
;     for (int j = 0; j < 4; ++j) { const int n = (lane >> 3) + 8 * j; const LAS float* s = scr + (8 * c) * 33 + n;
;         u32x4 o; o.x = cvtpk(s[0 * 33], s[1 * 33]); o.y = cvtpk(s[2 * 33], s[3 * 33]); o.z = cvtpk(s[4 * 33], s[5 * 33]); o.w = cvtpk(s[6 * 33], s[7 * 33]);
;         *(u32x4*)(dstrow0 + (size_t)n * ldt + k0 + 8 * c) = o; }
;     LDS_WAIT(); asm volatile("" ::: "memory");
; }
.LBB0_108:
	s_lshl_b32 s25, s22, 1
	s_lshl_b32 s39, s23, 1
	v_or_b32_e32 v4, s25, v1
	v_or_b32_e32 v7, s39, v2
	s_add_i32 s40, s25, 4
	s_add_i32 s41, s39, 4
	s_add_i32 s42, s25, 8
	s_add_i32 s43, s39, 8
	s_add_i32 s44, s25, 12
	s_add_i32 s45, s39, 12
	s_add_i32 s46, s25, 16
	s_add_i32 s47, s39, 16
	s_add_i32 s48, s25, 20
	s_add_i32 s49, s39, 20
	s_add_i32 s50, s25, 24
	s_add_i32 s51, s39, 24
	s_add_i32 s25, s25, 28
	s_add_i32 s39, s39, 28
	v_add_u32_e32 v25, s5, v4
	v_add_u32_e32 v27, s4, v7
	v_or_b32_e32 v62, s40, v1
	v_or_b32_e32 v63, s41, v2
	v_or_b32_e32 v64, s42, v1
	v_or_b32_e32 v65, s43, v2
	v_or_b32_e32 v66, s44, v1
	v_or_b32_e32 v67, s45, v2
	v_or_b32_e32 v68, s46, v1
	v_or_b32_e32 v69, s47, v2
	v_or_b32_e32 v70, s48, v1
	v_or_b32_e32 v71, s49, v2
	v_or_b32_e32 v72, s50, v1
	v_or_b32_e32 v73, s51, v2
	v_or_b32_e32 v74, s25, v1
	v_or_b32_e32 v75, s39, v2
	v_mad_i64_i32 v[30:31], s[40:41], v27, s38, v[28:29]
	v_mad_i64_i32 v[32:33], s[40:41], v25, s38, v[28:29]
	v_add_u32_e32 v25, s5, v62
	v_add_u32_e32 v27, s4, v63
	v_add_u32_e32 v40, s5, v64
	v_add_u32_e32 v38, s4, v65
	v_add_u32_e32 v44, s5, v66
	v_add_u32_e32 v42, s4, v67
	v_add_u32_e32 v48, s5, v68
	v_add_u32_e32 v46, s4, v69
	v_add_u32_e32 v52, s5, v70
	v_add_u32_e32 v50, s4, v71
	v_add_u32_e32 v56, s5, v72
	v_add_u32_e32 v54, s4, v73
	v_add_u32_e32 v60, s5, v74
	v_add_u32_e32 v58, s4, v75
	v_mad_i64_i32 v[34:35], s[40:41], v27, s38, v[28:29]
	v_mad_i64_i32 v[36:37], s[40:41], v25, s38, v[28:29]
	v_mad_i64_i32 v[38:39], s[40:41], v38, s38, v[28:29]
	v_mad_i64_i32 v[40:41], s[40:41], v40, s38, v[28:29]
	v_mad_i64_i32 v[42:43], s[40:41], v42, s38, v[28:29]
	v_mad_i64_i32 v[44:45], s[40:41], v44, s38, v[28:29]
	v_mad_i64_i32 v[46:47], s[40:41], v46, s38, v[28:29]
	v_mad_i64_i32 v[48:49], s[40:41], v48, s38, v[28:29]
	v_mad_i64_i32 v[50:51], s[40:41], v50, s38, v[28:29]
	v_mad_i64_i32 v[52:53], s[40:41], v52, s38, v[28:29]
	v_mad_i64_i32 v[54:55], s[40:41], v54, s38, v[28:29]
	v_mad_i64_i32 v[56:57], s[40:41], v56, s38, v[28:29]
	v_mad_i64_i32 v[58:59], s[40:41], v58, s38, v[28:29]
	v_mad_i64_i32 v[60:61], s[40:41], v60, s38, v[28:29]
	global_load_dword v25, v[30:31], off nt
	global_load_dword v27, v[32:33], off nt
	global_load_dword v76, v[34:35], off nt
	global_load_dword v77, v[36:37], off nt
	global_load_dword v78, v[38:39], off nt
	global_load_dword v79, v[40:41], off nt
	global_load_dword v80, v[42:43], off nt
	global_load_dword v81, v[44:45], off nt
	global_load_dword v82, v[46:47], off nt
	global_load_dword v83, v[48:49], off nt
	global_load_dword v84, v[50:51], off nt
	global_load_dword v85, v[52:53], off nt
	global_load_dword v86, v[54:55], off nt
	global_load_dword v87, v[56:57], off nt
	global_load_dword v88, v[58:59], off nt
	global_load_dword v89, v[60:61], off nt
	s_add_i32 s23, s23, 16
	s_add_i32 s22, s22, 16
	s_add_i32 s24, s24, -16
	v_mad_u64_u32 v[30:31], s[40:41], v7, s35, v[6:7]
	s_cmp_lg_u32 s24, 0
	v_mad_u64_u32 v[32:33], s[40:41], v4, s35, v[6:7]
	v_mad_u64_u32 v[34:35], s[40:41], v63, s35, v[6:7]
	v_mad_u64_u32 v[36:37], s[40:41], v62, s35, v[6:7]
	v_mad_u64_u32 v[38:39], s[40:41], v65, s35, v[6:7]
	v_mad_u64_u32 v[40:41], s[40:41], v64, s35, v[6:7]
	v_mad_u64_u32 v[42:43], s[40:41], v67, s35, v[6:7]
	v_mad_u64_u32 v[44:45], s[40:41], v66, s35, v[6:7]
	v_mad_u64_u32 v[46:47], s[40:41], v69, s35, v[6:7]
	v_mad_u64_u32 v[48:49], s[40:41], v68, s35, v[6:7]
	v_mad_u64_u32 v[50:51], s[40:41], v71, s35, v[6:7]
	v_mad_u64_u32 v[52:53], s[40:41], v70, s35, v[6:7]
	v_mad_u64_u32 v[54:55], s[40:41], v73, s35, v[6:7]
	v_mad_u64_u32 v[56:57], s[40:41], v72, s35, v[6:7]
	v_mad_u64_u32 v[58:59], s[40:41], v75, s35, v[6:7]
	v_mad_u64_u32 v[60:61], s[40:41], v74, s35, v[6:7]
	s_waitcnt vmcnt(15)
	ds_write_b32 v30, v25 offset:61440
	s_waitcnt vmcnt(14)
	ds_write_b32 v32, v27 offset:61440
	s_waitcnt vmcnt(13)
	ds_write_b32 v34, v76 offset:61440
	s_waitcnt vmcnt(12)
	ds_write_b32 v36, v77 offset:61440
	s_waitcnt vmcnt(11)
	ds_write_b32 v38, v78 offset:61440
	s_waitcnt vmcnt(10)
	ds_write_b32 v40, v79 offset:61440
	s_waitcnt vmcnt(9)
	ds_write_b32 v42, v80 offset:61440
	s_waitcnt vmcnt(8)
	ds_write_b32 v44, v81 offset:61440
	s_waitcnt vmcnt(7)
	ds_write_b32 v46, v82 offset:61440
	s_waitcnt vmcnt(6)
	ds_write_b32 v48, v83 offset:61440
	s_waitcnt vmcnt(5)
	ds_write_b32 v50, v84 offset:61440
	s_waitcnt vmcnt(4)
	ds_write_b32 v52, v85 offset:61440
	s_waitcnt vmcnt(3)
	ds_write_b32 v54, v86 offset:61440
	s_waitcnt vmcnt(2)
	ds_write_b32 v56, v87 offset:61440
	s_waitcnt vmcnt(1)
	ds_write_b32 v58, v88 offset:61440
	s_waitcnt vmcnt(0)
	ds_write_b32 v60, v89 offset:61440
	s_cbranch_scc1 .LBB0_108
	s_lshl_b64 s[18:19], s[18:19], 11
	s_waitcnt lgkmcnt(0)
	s_add_u32 s18, s20, s18
	s_addc_u32 s19, s21, s19
	s_ashr_i32 s5, s4, 31
	ds_read2_b32 v[32:33], v3 offset0:33 offset1:41
	ds_read2_b32 v[34:35], v3 offset1:8
	ds_read2_b32 v[36:37], v3 offset0:66 offset1:74
	ds_read2_b32 v[38:39], v3 offset0:99 offset1:107
	ds_read2_b32 v[40:41], v3 offset0:132 offset1:140
	ds_read2_b32 v[42:43], v3 offset0:165 offset1:173
	ds_read2_b32 v[44:45], v3 offset0:198 offset1:206
	ds_read2_b32 v[46:47], v3 offset0:231 offset1:239
	s_lshl_b64 s[4:5], s[4:5], 1
	s_add_u32 s4, s18, s4
	s_addc_u32 s5, s19, s5
	v_mov_b32_e32 v27, v5
	v_lshl_add_u64 v[48:49], s[4:5], 0, v[26:27]
	s_waitcnt lgkmcnt(6)
	v_cvt_pk_bf16_f32 v28, v34, v32
	s_waitcnt lgkmcnt(4)
	v_cvt_pk_bf16_f32 v29, v36, v38
	s_waitcnt lgkmcnt(2)
	v_cvt_pk_bf16_f32 v30, v40, v42
	s_waitcnt lgkmcnt(0)
	v_cvt_pk_bf16_f32 v31, v44, v46
	v_lshl_add_u64 v[50:51], v[48:49], 0, v[8:9]
	global_store_dwordx4 v[50:51], v[28:31], off
	s_nop 1
	v_cvt_pk_bf16_f32 v28, v35, v33
	v_cvt_pk_bf16_f32 v29, v37, v39
	v_cvt_pk_bf16_f32 v30, v41, v43
	v_cvt_pk_bf16_f32 v31, v45, v47
	ds_read2_b32 v[34:35], v3 offset0:49 offset1:57
	ds_read2_b32 v[36:37], v3 offset0:16 offset1:24
	ds_read2_b32 v[38:39], v3 offset0:82 offset1:90
	ds_read2_b32 v[40:41], v3 offset0:115 offset1:123
	ds_read2_b32 v[42:43], v3 offset0:148 offset1:156
	ds_read2_b32 v[44:45], v3 offset0:181 offset1:189
	ds_read2_b32 v[46:47], v3 offset0:214 offset1:222
	ds_read2_b32 v[50:51], v3 offset0:247 offset1:255
	v_lshl_add_u64 v[32:33], v[48:49], 0, v[10:11]
	global_store_dwordx4 v[32:33], v[28:31], off
	v_lshl_add_u64 v[32:33], v[48:49], 0, v[12:13]
	s_waitcnt lgkmcnt(6)
	v_cvt_pk_bf16_f32 v28, v36, v34
	s_waitcnt lgkmcnt(4)
	v_cvt_pk_bf16_f32 v29, v38, v40
	s_waitcnt lgkmcnt(2)
	v_cvt_pk_bf16_f32 v30, v42, v44
	s_waitcnt lgkmcnt(0)
	v_cvt_pk_bf16_f32 v31, v46, v50
	global_store_dwordx4 v[32:33], v[28:31], off
	v_lshl_add_u64 v[32:33], v[48:49], 0, v[14:15]
	s_nop 0
	v_cvt_pk_bf16_f32 v28, v37, v35
	v_cvt_pk_bf16_f32 v29, v39, v41
	v_cvt_pk_bf16_f32 v30, v43, v45
	v_cvt_pk_bf16_f32 v31, v47, v51
	global_store_dwordx4 v[32:33], v[28:31], off
	s_waitcnt lgkmcnt(0)
	s_branch .LBB0_62
